# COMB: per-row parameter loads (g2, norm gain/shift/scale, final gain) issued together into fresh registers and copied back after their waits; rows 1-2 slot tables loaded with row 0's, serialising vmcn
# speedup vs baseline: 1.0053x; 1.0053x over previous
.LBB0_2151:
	v_readlane_b32 s8, v253, 53
	s_add_i32 s9, s8, s39
	s_min_i32 s26, s9, s40
	s_ashr_i32 s27, s26, 31
	s_lshl_b64 s[10:11], s[26:27], 4
	v_readlane_b32 s23, v253, 0
	s_add_u32 s30, s23, s10
	v_readlane_b32 s43, v253, 1
	s_addc_u32 s31, s43, s11
	v_readlane_b32 s46, v253, 2
	s_add_u32 s10, s46, s10
	v_readlane_b32 s47, v253, 3
	s_addc_u32 s11, s47, s11
	v_readlane_b32 s8, v252, 37
	global_load_dwordx4 v[10:13], v1, s[10:11]
	s_add_i32 s10, s8, s39
	s_min_i32 s34, s10, s40
	s_ashr_i32 s35, s34, 31
	s_lshl_b64 s[12:13], s[34:35], 4
	s_add_u32 s36, s23, s12
	s_addc_u32 s37, s43, s13
	s_add_u32 s12, s46, s12
	s_addc_u32 s13, s47, s13
	global_load_dwordx4 v[6:9], v1, s[12:13]
	v_readlane_b32 s12, v252, 9
	s_add_i32 s8, s12, s39
	s_min_i32 s28, s8, s40
	s_ashr_i32 s29, s28, 31
	s_lshl_b64 s[44:45], s[28:29], 4
	v_readlane_b32 s13, v252, 10
	s_add_u32 s12, s23, s44
	s_addc_u32 s13, s43, s45
	s_add_u32 s44, s46, s44
	s_addc_u32 s45, s47, s45
	s_lshl_b64 s[26:27], s[26:27], 11
	v_lshl_add_u64 v[48:49], v[32:33], 0, s[26:27]
	global_load_dwordx4 v[2:5], v1, s[44:45]
	global_load_dwordx2 v[70:71], v[48:49], off
	global_load_dwordx4 v[14:17], v1, s[30:31]
	global_load_dwordx4 v[216:219], v1, s[36:37]
	global_load_dwordx4 v[220:223], v1, s[12:13]
	v_readlane_b32 s48, v253, 6
	v_readlane_b32 s49, v253, 7
	v_lshlrev_b32_e32 v19, 2, v24
	s_mov_b32 s11, 0x3a4000
	v_lshlrev_b32_e32 v129, 4, v24
	v_lshlrev_b32_e32 v134, 4, v26
	v_lshlrev_b32_e32 v147, 4, v20
	s_waitcnt vmcnt(0)
	v_ashrrev_i32_e32 v51, 31, v14
	v_mov_b32_e32 v50, v14
	v_ashrrev_i32_e32 v53, 31, v15
	v_mov_b32_e32 v52, v15
	v_lshlrev_b64 v[50:51], 10, v[50:51]
	v_lshlrev_b64 v[14:15], 10, v[52:53]
	v_lshl_add_u64 v[52:53], v[22:23], 0, v[50:51]
	global_load_dword v83, v[52:53], off
	v_lshl_add_u64 v[52:53], v[22:23], 0, v[14:15]
	global_load_dword v166, v[52:53], off
	v_ashrrev_i32_e32 v53, 31, v16
	v_mov_b32_e32 v52, v16
	v_ashrrev_i32_e32 v55, 31, v17
	v_mov_b32_e32 v54, v17
	v_lshlrev_b64 v[52:53], 10, v[52:53]
	v_lshl_add_u64 v[14:15], s[48:49], 0, v[14:15]
	v_lshlrev_b64 v[16:17], 10, v[54:55]
	v_readfirstlane_b32 s30, v14
	v_readfirstlane_b32 s31, v15
	v_lshl_add_u64 v[14:15], s[48:49], 0, v[52:53]
	v_lshl_add_u64 v[54:55], v[22:23], 0, v[52:53]
	v_lshl_add_u64 v[50:51], s[48:49], 0, v[50:51]
	v_readfirstlane_b32 s44, v14
	v_readfirstlane_b32 s45, v15
	v_lshl_add_u64 v[14:15], s[48:49], 0, v[16:17]
	global_load_dword v167, v[54:55], off
	v_lshl_add_u64 v[54:55], v[22:23], 0, v[16:17]
	v_readfirstlane_b32 s26, v50
	v_readfirstlane_b32 s27, v51
	v_readfirstlane_b32 s46, v14
	v_readfirstlane_b32 s47, v15
	v_lshlrev_b32_e32 v16, 2, v26
	v_lshlrev_b32_e32 v17, 2, v20
	global_load_dword v168, v[54:55], off
	global_load_dwordx2 v[68:69], v[48:49], off offset:512
	global_load_dword v87, v19, s[26:27]
	global_load_dword v89, v19, s[30:31]
	global_load_dword v164, v19, s[44:45]
	global_load_dword v165, v19, s[46:47]
	global_load_dwordx2 v[66:67], v[48:49], off offset:1024
	global_load_dword v163, v16, s[26:27]
	global_load_dword v162, v16, s[30:31]
	global_load_dword v161, v16, s[44:45]
	global_load_dword v160, v16, s[46:47]
	global_load_dwordx2 v[64:65], v[48:49], off offset:1536
	global_load_dword v159, v17, s[26:27]
	global_load_dword v158, v17, s[30:31]
	global_load_dword v157, v17, s[44:45]
	global_load_dword v156, v17, s[46:47]
	s_lshl_b64 s[26:27], s[34:35], 11
	v_lshl_add_u64 v[14:15], v[32:33], 0, s[26:27]
	global_load_dwordx2 v[62:63], v[14:15], off
	v_readlane_b32 s44, v252, 4
	v_readlane_b32 s45, v252, 5
	v_mov_b64_e32 v[48:49], v[216:217]
	v_mov_b64_e32 v[50:51], v[218:219]
	v_ashrrev_i32_e32 v53, 31, v48
	v_mov_b32_e32 v52, v48
	v_ashrrev_i32_e32 v55, 31, v49
	v_mov_b32_e32 v54, v49
	v_lshlrev_b64 v[52:53], 10, v[52:53]
	v_lshlrev_b64 v[48:49], 10, v[54:55]
	v_lshl_add_u64 v[54:55], v[22:23], 0, v[52:53]
	global_load_dword v152, v[54:55], off
	v_lshl_add_u64 v[54:55], v[22:23], 0, v[48:49]
	global_load_dword v153, v[54:55], off
	v_ashrrev_i32_e32 v55, 31, v50
	v_mov_b32_e32 v54, v50
	v_ashrrev_i32_e32 v57, 31, v51
	v_mov_b32_e32 v56, v51
	v_lshlrev_b64 v[54:55], 10, v[54:55]
	v_lshl_add_u64 v[48:49], s[48:49], 0, v[48:49]
	v_lshlrev_b64 v[50:51], 10, v[56:57]
	v_readfirstlane_b32 s30, v48
	v_readfirstlane_b32 s31, v49
	v_lshl_add_u64 v[48:49], s[48:49], 0, v[54:55]
	v_lshl_add_u64 v[56:57], v[22:23], 0, v[54:55]
	v_lshl_add_u64 v[52:53], s[48:49], 0, v[52:53]
	v_readfirstlane_b32 s34, v48
	v_readfirstlane_b32 s35, v49
	v_lshl_add_u64 v[48:49], s[48:49], 0, v[50:51]
	global_load_dword v154, v[56:57], off
	v_lshl_add_u64 v[56:57], v[22:23], 0, v[50:51]
	v_readfirstlane_b32 s26, v52
	v_readfirstlane_b32 s27, v53
	v_readfirstlane_b32 s36, v48
	v_readfirstlane_b32 s37, v49
	global_load_dword v155, v[56:57], off
	global_load_dwordx2 v[60:61], v[14:15], off offset:512
	global_load_dword v149, v19, s[30:31]
	global_load_dword v148, v19, s[26:27]
	global_load_dword v150, v19, s[34:35]
	global_load_dword v151, v19, s[36:37]
	global_load_dwordx2 v[58:59], v[14:15], off offset:1024
	global_load_dword v146, v16, s[26:27]
	global_load_dword v145, v16, s[30:31]
	global_load_dword v144, v16, s[34:35]
	global_load_dword v143, v16, s[36:37]
	global_load_dwordx2 v[56:57], v[14:15], off offset:1536
	global_load_dword v142, v17, s[26:27]
	global_load_dword v141, v17, s[30:31]
	global_load_dword v140, v17, s[34:35]
	global_load_dword v139, v17, s[36:37]
	s_lshl_b64 s[26:27], s[28:29], 11
	v_lshl_add_u64 v[14:15], v[32:33], 0, s[26:27]
	global_load_dwordx2 v[48:49], v[14:15], off
	v_mov_b64_e32 v[50:51], v[220:221]
	v_mov_b64_e32 v[52:53], v[222:223]
	v_ashrrev_i32_e32 v55, 31, v50
	v_mov_b32_e32 v54, v50
	v_ashrrev_i32_e32 v73, 31, v51
	v_mov_b32_e32 v72, v51
	v_lshlrev_b64 v[50:51], 10, v[72:73]
	v_lshlrev_b64 v[72:73], 10, v[54:55]
	v_lshl_add_u64 v[54:55], v[22:23], 0, v[72:73]
	global_load_dword v135, v[54:55], off
	v_lshl_add_u64 v[54:55], v[22:23], 0, v[50:51]
	global_load_dword v136, v[54:55], off
	v_ashrrev_i32_e32 v55, 31, v52
	v_mov_b32_e32 v54, v52
	v_ashrrev_i32_e32 v75, 31, v53
	v_mov_b32_e32 v74, v53
	v_lshlrev_b64 v[52:53], 10, v[74:75]
	v_lshlrev_b64 v[74:75], 10, v[54:55]
	v_lshl_add_u64 v[50:51], s[48:49], 0, v[50:51]
	v_lshl_add_u64 v[54:55], v[22:23], 0, v[74:75]
	v_readfirstlane_b32 s26, v50
	v_readfirstlane_b32 s27, v51
	v_lshl_add_u64 v[50:51], s[48:49], 0, v[74:75]
	v_lshl_add_u64 v[72:73], s[48:49], 0, v[72:73]
	v_readfirstlane_b32 s28, v50
	v_readfirstlane_b32 s29, v51
	v_lshl_add_u64 v[50:51], s[48:49], 0, v[52:53]
	global_load_dword v137, v[54:55], off
	v_lshl_add_u64 v[54:55], v[22:23], 0, v[52:53]
	v_readfirstlane_b32 s12, v72
	v_readfirstlane_b32 s13, v73
	v_readfirstlane_b32 s30, v50
	v_readfirstlane_b32 s31, v51
	global_load_dword v138, v[54:55], off
	s_nop 0
	global_load_dwordx2 v[54:55], v[14:15], off offset:512
	global_load_dword v130, v19, s[12:13]
	global_load_dword v131, v19, s[26:27]
	global_load_dword v132, v19, s[28:29]
	global_load_dword v133, v19, s[30:31]
	global_load_dwordx2 v[52:53], v[14:15], off offset:1024
	global_load_dword v128, v16, s[12:13]
	global_load_dword v127, v16, s[26:27]
	global_load_dword v126, v16, s[28:29]
	global_load_dword v125, v16, s[30:31]
	global_load_dwordx2 v[50:51], v[14:15], off offset:1536
	global_load_dword v124, v17, s[12:13]
	global_load_dword v27, v17, s[26:27]
	global_load_dword v25, v17, s[28:29]
	global_load_dword v21, v17, s[30:31]
	s_add_u32 s12, s44, s4
	s_addc_u32 s13, s45, s5
	v_mov_b32_e32 v14, 0x27c000
	global_load_dwordx4 v[76:79], v14, s[12:13]
	s_waitcnt vmcnt(0)
	v_ashrrev_i32_e32 v15, 31, v79
	v_mov_b32_e32 v14, v79
	v_ashrrev_i32_e32 v79, 31, v78
	v_lshlrev_b64 v[74:75], 10, v[14:15]
	v_lshlrev_b64 v[72:73], 10, v[78:79]
	v_lshl_add_u64 v[14:15], s[48:49], 0, v[74:75]
	v_lshl_add_u64 v[74:75], v[22:23], 0, v[74:75]
	v_readfirstlane_b32 s28, v14
	v_readfirstlane_b32 s29, v15
	v_lshl_add_u64 v[14:15], s[48:49], 0, v[72:73]
	v_lshl_add_u64 v[72:73], v[22:23], 0, v[72:73]
	v_readfirstlane_b32 s30, v14
	v_readfirstlane_b32 s31, v15
	v_ashrrev_i32_e32 v15, 31, v77
	v_mov_b32_e32 v14, v77
	v_ashrrev_i32_e32 v77, 31, v76
	v_lshlrev_b64 v[80:81], 10, v[14:15]
	v_lshlrev_b64 v[78:79], 10, v[76:77]
	v_lshl_add_u64 v[14:15], s[48:49], 0, v[80:81]
	v_lshl_add_u64 v[76:77], s[44:45], 0, v[40:41]
	v_readfirstlane_b32 s34, v14
	v_readfirstlane_b32 s35, v15
	v_lshl_add_u64 v[14:15], s[48:49], 0, v[78:79]
	v_add_co_u32_e32 v92, vcc, s11, v76
	v_readfirstlane_b32 s36, v14
	v_readfirstlane_b32 s37, v15
	v_addc_co_u32_e32 v93, vcc, 0, v77, vcc
	global_load_dword v85, v17, s[28:29]
	global_load_dword v110, v17, s[30:31]
	global_load_dword v108, v17, s[34:35]
	s_nop 0
	global_load_dword v109, v17, s[36:37]
	global_load_dwordx2 v[14:15], v[92:93], off offset:2048
	global_load_dword v111, v16, s[28:29]
	global_load_dword v116, v16, s[30:31]
	global_load_dword v114, v16, s[34:35]
	global_load_dword v115, v16, s[36:37]
	s_nop 0
	global_load_dwordx2 v[16:17], v[92:93], off offset:1536
	global_load_dword v106, v19, s[28:29]
	global_load_dword v104, v19, s[30:31]
	global_load_dword v105, v19, s[34:35]
	global_load_dword v107, v19, s[36:37]
	global_load_dwordx2 v[90:91], v[92:93], off offset:1024
	global_load_dword v96, v[72:73], off
	v_lshl_add_u64 v[72:73], v[22:23], 0, v[80:81]
	global_load_dword v19, v[74:75], off
	global_load_dword v94, v[72:73], off
	v_lshl_add_u64 v[72:73], v[22:23], 0, v[78:79]
	global_load_dword v80, v[72:73], off
	global_load_dwordx2 v[78:79], v[92:93], off offset:512
	v_mov_b32_e32 v72, 0x1f4000
	global_load_dwordx4 v[72:75], v72, s[12:13]
	s_ashr_i32 s11, s39, 31
	s_lshr_b32 s11, s11, 20
	s_add_i32 s11, s39, s11
	s_ashr_i32 s11, s11, 12
	s_cmp_lt_i32 s39, 0x8000
	s_cselect_b32 s11, s11, 8
	s_ashr_i32 s23, s11, 31
	s_add_u32 s12, s11, s41
	s_addc_u32 s13, s23, 0
	s_mulk_i32 s13, 0x6000
	s_mul_hi_u32 s26, s12, 0x6000
	s_add_i32 s26, s26, s13
	s_mulk_i32 s12, 0x6000
	s_add_u32 s12, s44, s12
	s_addc_u32 s13, s45, s26
	s_add_u32 s12, s12, 0x105000
	s_addc_u32 s13, s13, 0
	v_readlane_b32 s26, v254, 44
	v_readlane_b32 s27, v254, 45
	s_waitcnt vmcnt(16)
	v_lshlrev_b32_e32 v122, 16, v14
	v_and_b32_e32 v123, 0xffff0000, v14
	v_lshlrev_b32_e32 v120, 16, v15
	v_and_b32_e32 v121, 0xffff0000, v15
	s_waitcnt vmcnt(11)
	v_lshlrev_b32_e32 v118, 16, v16
	v_and_b32_e32 v119, 0xffff0000, v16
	v_lshlrev_b32_e32 v16, 16, v17
	v_and_b32_e32 v17, 0xffff0000, v17
	s_waitcnt vmcnt(6)
	v_lshlrev_b32_e32 v112, 16, v90
	v_and_b32_e32 v113, 0xffff0000, v90
	v_lshlrev_b32_e32 v90, 16, v91
	s_waitcnt vmcnt(4)
	v_cvt_pk_f32_fp8_e32 v[98:99], v19
	s_waitcnt vmcnt(3)
	v_cvt_pk_f32_fp8_sdwa v[92:93], v94 src0_sel:WORD_1
	v_cvt_pk_f32_fp8_sdwa v[100:101], v19 src0_sel:WORD_1
	v_lshlrev_b32_e32 v19, 4, v18
	s_waitcnt vmcnt(1)
	v_lshlrev_b32_e32 v102, 16, v78
	s_waitcnt vmcnt(0)
	v_mul_f32_e32 v88, 0x3e000000, v72
	v_mul_f32_e32 v86, 0x3e000000, v73
	v_cvt_pk_f32_fp8_e32 v[72:73], v80
	v_mul_f32_e32 v84, 0x3e000000, v74
	v_mul_f32_e32 v82, 0x3e000000, v75
	v_cvt_pk_f32_fp8_e32 v[74:75], v94
	v_cvt_pk_f32_fp8_e32 v[94:95], v96
	v_pk_fma_f32 v[72:73], v[88:89], v[72:73], 0 op_sel_hi:[0,1,0]
	v_cvt_pk_f32_fp8_sdwa v[80:81], v80 src0_sel:WORD_1
	v_pk_fma_f32 v[72:73], v[86:87], v[74:75], v[72:73] op_sel_hi:[0,1,1]
	v_pk_fma_f32 v[72:73], v[84:85], v[94:95], v[72:73] op_sel_hi:[0,1,1]
	v_pk_fma_f32 v[94:95], v[82:83], v[98:99], v[72:73] op_sel_hi:[0,1,1]
	global_load_dwordx4 v[72:75], v19, s[12:13]
	global_load_dwordx4 v[170:173], v129, s[12:13]
	global_load_dwordx4 v[174:177], v134, s[12:13]
	global_load_dwordx4 v[178:181], v147, s[12:13]
	v_cvt_pk_f32_fp8_sdwa v[96:97], v96 src0_sel:WORD_1
	v_pk_fma_f32 v[80:81], v[88:89], v[80:81], 0 op_sel_hi:[0,1,0]
	v_pk_fma_f32 v[80:81], v[86:87], v[92:93], v[80:81] op_sel_hi:[0,1,1]
	v_and_b32_e32 v103, 0xffff0000, v78
	v_pk_fma_f32 v[80:81], v[84:85], v[96:97], v[80:81] op_sel_hi:[0,1,1]
	v_lshlrev_b32_e32 v78, 16, v79
	v_and_b32_e32 v79, 0xffff0000, v79
	v_pk_fma_f32 v[80:81], v[82:83], v[100:101], v[80:81] op_sel_hi:[0,1,1]
	v_cvt_pk_f32_fp8_e32 v[100:101], v104
	v_cvt_pk_f32_fp8_sdwa v[98:99], v105 src0_sel:WORD_1
	v_cvt_pk_f32_fp8_sdwa v[92:93], v107 src0_sel:WORD_1
	v_and_b32_e32 v91, 0xffff0000, v91
	v_pk_fma_f32 v[92:93], v[88:89], v[92:93], 0 op_sel_hi:[0,1,0]
	v_pk_fma_f32 v[92:93], v[86:87], v[98:99], v[92:93] op_sel_hi:[0,1,1]
	s_waitcnt vmcnt(0)
	v_pk_fma_f32 v[74:75], v[80:81], v[74:75], v[78:79]
	v_cvt_pk_f32_fp8_e32 v[78:79], v107
	v_cvt_pk_f32_fp8_e32 v[80:81], v105
	v_pk_fma_f32 v[72:73], v[72:73], v[94:95], v[102:103]
	v_cvt_pk_f32_fp8_sdwa v[102:103], v104 src0_sel:WORD_1
	v_cvt_pk_f32_fp8_e32 v[104:105], v106
	v_pk_fma_f32 v[78:79], v[88:89], v[78:79], 0 op_sel_hi:[0,1,0]
	v_pk_fma_f32 v[78:79], v[86:87], v[80:81], v[78:79] op_sel_hi:[0,1,1]
	v_pk_fma_f32 v[78:79], v[84:85], v[100:101], v[78:79] op_sel_hi:[0,1,1]
	v_pk_fma_f32 v[100:101], v[82:83], v[104:105], v[78:79] op_sel_hi:[0,1,1]
	v_cvt_pk_f32_fp8_sdwa v[106:107], v106 src0_sel:WORD_1
	v_pk_fma_f32 v[92:93], v[84:85], v[102:103], v[92:93] op_sel_hi:[0,1,1]
	v_cvt_pk_f32_fp8_sdwa v[102:103], v114 src0_sel:WORD_1
	v_cvt_pk_f32_fp8_sdwa v[104:105], v116 src0_sel:WORD_1
	v_pk_fma_f32 v[92:93], v[82:83], v[106:107], v[92:93] op_sel_hi:[0,1,1]
	v_cvt_pk_f32_fp8_sdwa v[106:107], v111 src0_sel:WORD_1
	v_pk_mul_f32 v[96:97], v[72:73], v[72:73]
	v_pk_mul_f32 v[94:95], v[74:75], v[74:75]
	s_waitcnt vmcnt(0)
	v_mov_b64_e32 v[78:79], v[170:171]
	v_mov_b64_e32 v[80:81], v[172:173]
	v_pk_fma_f32 v[80:81], v[92:93], v[80:81], v[90:91]
	v_cvt_pk_f32_fp8_e32 v[90:91], v115
	v_pk_fma_f32 v[78:79], v[78:79], v[100:101], v[112:113]
	v_cvt_pk_f32_fp8_e32 v[112:113], v114
	v_cvt_pk_f32_fp8_sdwa v[92:93], v115 src0_sel:WORD_1
	v_cvt_pk_f32_fp8_e32 v[114:115], v116
	v_pk_fma_f32 v[90:91], v[88:89], v[90:91], 0 op_sel_hi:[0,1,0]
	v_pk_fma_f32 v[90:91], v[86:87], v[112:113], v[90:91] op_sel_hi:[0,1,1]
	v_pk_fma_f32 v[92:93], v[88:89], v[92:93], 0 op_sel_hi:[0,1,0]
	v_pk_fma_f32 v[90:91], v[84:85], v[114:115], v[90:91] op_sel_hi:[0,1,1]
	v_pk_fma_f32 v[92:93], v[86:87], v[102:103], v[92:93] op_sel_hi:[0,1,1]
	v_cvt_pk_f32_fp8_e32 v[116:117], v111
	v_pk_fma_f32 v[92:93], v[84:85], v[104:105], v[92:93] op_sel_hi:[0,1,1]
	v_pk_fma_f32 v[92:93], v[82:83], v[106:107], v[92:93] op_sel_hi:[0,1,1]
	v_cvt_pk_f32_fp8_sdwa v[106:107], v109 src0_sel:WORD_1
	v_pk_fma_f32 v[90:91], v[82:83], v[116:117], v[90:91] op_sel_hi:[0,1,1]
	v_cvt_pk_f32_fp8_e32 v[116:117], v110
	v_cvt_pk_f32_fp8_sdwa v[110:111], v110 src0_sel:WORD_1
	v_pk_fma_f32 v[106:107], v[88:89], v[106:107], 0 op_sel_hi:[0,1,0]
	v_pk_mul_f32 v[100:101], v[78:79], v[78:79]
	v_pk_mul_f32 v[98:99], v[80:81], v[80:81]
	s_waitcnt vmcnt(0)
	v_mov_b64_e32 v[112:113], v[174:175]
	v_mov_b64_e32 v[114:115], v[176:177]
	v_pk_fma_f32 v[92:93], v[92:93], v[114:115], v[16:17]
	v_cvt_pk_f32_fp8_e32 v[16:17], v109
	v_cvt_pk_f32_fp8_e32 v[114:115], v108
	v_pk_fma_f32 v[90:91], v[112:113], v[90:91], v[118:119]
	v_cvt_pk_f32_fp8_e32 v[118:119], v85
	v_pk_fma_f32 v[14:15], v[88:89], v[16:17], 0 op_sel_hi:[0,1,0]
	v_pk_fma_f32 v[14:15], v[86:87], v[114:115], v[14:15] op_sel_hi:[0,1,1]
	v_pk_fma_f32 v[14:15], v[84:85], v[116:117], v[14:15] op_sel_hi:[0,1,1]
	v_pk_fma_f32 v[114:115], v[82:83], v[118:119], v[14:15] op_sel_hi:[0,1,1]
	v_cvt_pk_f32_fp8_sdwa v[108:109], v108 src0_sel:WORD_1
	v_cvt_pk_f32_fp8_sdwa v[112:113], v85 src0_sel:WORD_1
	v_pk_mul_f32 v[104:105], v[90:91], v[90:91]
	v_pk_mul_f32 v[102:103], v[92:93], v[92:93]
	v_pk_fma_f32 v[106:107], v[86:87], v[108:109], v[106:107] op_sel_hi:[0,1,1]
	v_pk_fma_f32 v[84:85], v[84:85], v[110:111], v[106:107] op_sel_hi:[0,1,1]
	v_pk_fma_f32 v[84:85], v[82:83], v[112:113], v[84:85] op_sel_hi:[0,1,1]
	v_add_f32_e32 v82, v100, v101
	v_add_f32_e32 v86, v96, v97
	v_add_f32_e32 v82, v82, v98
	v_add_f32_e32 v86, v86, v94
	v_add_f32_e32 v82, v99, v82
	v_add_f32_e32 v86, v95, v86
	v_add_f32_e32 v82, v86, v82
	v_add_f32_e32 v86, v104, v105
	v_add_f32_e32 v86, v86, v102
	v_add_f32_e32 v86, v103, v86
	v_add_f32_e32 v82, v82, v86
	s_mov_b32 s12, 0x800000
	s_waitcnt vmcnt(0)
	v_mov_b64_e32 v[14:15], v[178:179]
	v_mov_b64_e32 v[16:17], v[180:181]
	v_pk_fma_f32 v[14:15], v[14:15], v[114:115], v[122:123]
	v_pk_fma_f32 v[16:17], v[84:85], v[16:17], v[120:121]
	v_pk_mul_f32 v[84:85], v[14:15], v[14:15]
	v_pk_mul_f32 v[106:107], v[16:17], v[16:17]
	v_add_f32_e32 v84, v84, v85
	v_add_f32_e32 v84, v84, v106
	v_add_f32_e32 v84, v107, v84
	v_add_f32_e32 v82, v82, v84
	s_nop 1
	v_add_f32_dpp v82, v82, v82 row_ror:1 row_mask:0xf bank_mask:0xf bound_ctrl:1
	s_nop 1
	v_add_f32_dpp v82, v82, v82 row_ror:2 row_mask:0xf bank_mask:0xf bound_ctrl:1
	s_nop 1
	v_add_f32_dpp v82, v82, v82 row_ror:4 row_mask:0xf bank_mask:0xf bound_ctrl:1
	s_nop 1
	v_add_f32_dpp v82, v82, v82 row_ror:8 row_mask:0xf bank_mask:0xf bound_ctrl:1
	v_mov_b32_e32 v84, v82
	s_nop 1
	v_permlane16_swap_b32_e32 v82, v84
	v_add_f32_e32 v82, v82, v84
	v_mov_b32_e32 v84, v82
	s_nop 1
	v_permlane32_swap_b32_e32 v82, v84
	v_add_f32_e32 v82, v82, v84
	v_fmamk_f32 v82, v82, 0x3a800000, v237
	v_cmp_gt_f32_e32 vcc, s12, v82
	v_mul_f32_e32 v84, 0x4b800000, v82
	s_mov_b64 s[12:13], -1
	v_cndmask_b32_e32 v82, v82, v84, vcc
	v_rsq_f32_e32 v82, v82
	s_nop 0
	v_mul_f32_e32 v84, 0x45800000, v82
	v_cndmask_b32_e32 v82, v82, v84, vcc
	s_andn2_b64 vcc, exec, s[26:27]
	s_cbranch_vccnz .LBB0_2153
	v_and_b32_sdwa v100, v75, v236 dst_sel:DWORD dst_unused:UNUSED_PAD src0_sel:WORD_1 src1_sel:DWORD
	v_and_b32_sdwa v101, v73, v236 dst_sel:DWORD dst_unused:UNUSED_PAD src0_sel:WORD_1 src1_sel:DWORD
	v_and_b32_sdwa v86, v74, v236 dst_sel:DWORD dst_unused:UNUSED_PAD src0_sel:WORD_1 src1_sel:DWORD
	v_and_b32_sdwa v88, v72, v236 dst_sel:DWORD dst_unused:UNUSED_PAD src0_sel:WORD_1 src1_sel:DWORD
	v_add3_u32 v100, v75, v100, s80
	v_add3_u32 v101, v73, v101, s80
	s_mov_b64 s[12:13], 0x3a4200
	v_add3_u32 v88, v72, v88, s80
	v_add3_u32 v86, v74, v86, s80
	v_and_b32_e32 v100, 0xffff0000, v100
	v_and_b32_e32 v102, 0xffff0000, v101
	v_lshl_add_u64 v[84:85], v[76:77], 0, s[12:13]
	v_or_b32_sdwa v101, v100, v86 dst_sel:DWORD dst_unused:UNUSED_PAD src0_sel:DWORD src1_sel:WORD_1
	v_or_b32_sdwa v100, v102, v88 dst_sel:DWORD dst_unused:UNUSED_PAD src0_sel:DWORD src1_sel:WORD_1
	global_store_dwordx2 v[84:85], v[100:101], off
	v_and_b32_sdwa v85, v78, v236 dst_sel:DWORD dst_unused:UNUSED_PAD src0_sel:WORD_1 src1_sel:DWORD
	s_mov_b64 s[12:13], 0x3a4800
	v_add3_u32 v86, v78, v85, s80
	v_and_b32_sdwa v85, v81, v236 dst_sel:DWORD dst_unused:UNUSED_PAD src0_sel:WORD_1 src1_sel:DWORD
	v_and_b32_sdwa v88, v79, v236 dst_sel:DWORD dst_unused:UNUSED_PAD src0_sel:WORD_1 src1_sel:DWORD
	v_lshl_add_u64 v[94:95], v[76:77], 0, s[12:13]
	s_mov_b64 s[12:13], 0x3a4600
	v_and_b32_sdwa v84, v80, v236 dst_sel:DWORD dst_unused:UNUSED_PAD src0_sel:WORD_1 src1_sel:DWORD
	v_add3_u32 v85, v81, v85, s80
	v_add3_u32 v88, v79, v88, s80
	v_lshl_add_u64 v[96:97], v[76:77], 0, s[12:13]
	s_mov_b64 s[12:13], 0x3a4400
	v_add3_u32 v84, v80, v84, s80
	v_and_b32_e32 v85, 0xffff0000, v85
	v_and_b32_e32 v88, 0xffff0000, v88
	v_lshl_add_u64 v[98:99], v[76:77], 0, s[12:13]
	v_or_b32_sdwa v85, v85, v84 dst_sel:DWORD dst_unused:UNUSED_PAD src0_sel:DWORD src1_sel:WORD_1
	v_or_b32_sdwa v84, v88, v86 dst_sel:DWORD dst_unused:UNUSED_PAD src0_sel:DWORD src1_sel:WORD_1
	global_store_dwordx2 v[98:99], v[84:85], off
	v_and_b32_sdwa v85, v90, v236 dst_sel:DWORD dst_unused:UNUSED_PAD src0_sel:WORD_1 src1_sel:DWORD
	v_add3_u32 v86, v90, v85, s80
	v_and_b32_sdwa v85, v93, v236 dst_sel:DWORD dst_unused:UNUSED_PAD src0_sel:WORD_1 src1_sel:DWORD
	v_and_b32_sdwa v88, v91, v236 dst_sel:DWORD dst_unused:UNUSED_PAD src0_sel:WORD_1 src1_sel:DWORD
	v_and_b32_sdwa v84, v92, v236 dst_sel:DWORD dst_unused:UNUSED_PAD src0_sel:WORD_1 src1_sel:DWORD
	v_add3_u32 v85, v93, v85, s80
	v_add3_u32 v88, v91, v88, s80
	v_add3_u32 v84, v92, v84, s80
	v_and_b32_e32 v85, 0xffff0000, v85
	v_and_b32_e32 v88, 0xffff0000, v88
	s_add_u32 s11, s11, s42
	v_or_b32_sdwa v85, v85, v84 dst_sel:DWORD dst_unused:UNUSED_PAD src0_sel:DWORD src1_sel:WORD_1
	v_or_b32_sdwa v84, v88, v86 dst_sel:DWORD dst_unused:UNUSED_PAD src0_sel:DWORD src1_sel:WORD_1
	s_addc_u32 s12, s23, 0
	global_store_dwordx2 v[96:97], v[84:85], off
	v_and_b32_sdwa v85, v14, v236 dst_sel:DWORD dst_unused:UNUSED_PAD src0_sel:WORD_1 src1_sel:DWORD
	s_mulk_i32 s12, 0x6000
	s_mul_hi_u32 s13, s11, 0x6000
	v_add3_u32 v86, v14, v85, s80
	v_and_b32_sdwa v85, v17, v236 dst_sel:DWORD dst_unused:UNUSED_PAD src0_sel:WORD_1 src1_sel:DWORD
	v_and_b32_sdwa v88, v15, v236 dst_sel:DWORD dst_unused:UNUSED_PAD src0_sel:WORD_1 src1_sel:DWORD
	s_add_i32 s13, s13, s12
	s_mulk_i32 s11, 0x6000
	v_readlane_b32 s12, v253, 8
	v_and_b32_sdwa v84, v16, v236 dst_sel:DWORD dst_unused:UNUSED_PAD src0_sel:WORD_1 src1_sel:DWORD
	v_add3_u32 v85, v17, v85, s80
	v_add3_u32 v88, v15, v88, s80
	s_add_u32 s12, s12, s11
	v_readlane_b32 s11, v253, 9
	v_add3_u32 v84, v16, v84, s80
	v_and_b32_e32 v85, 0xffff0000, v85
	v_and_b32_e32 v88, 0xffff0000, v88
	s_addc_u32 s13, s11, s13
	v_or_b32_sdwa v85, v85, v84 dst_sel:DWORD dst_unused:UNUSED_PAD src0_sel:DWORD src1_sel:WORD_1
	v_or_b32_sdwa v84, v88, v86 dst_sel:DWORD dst_unused:UNUSED_PAD src0_sel:DWORD src1_sel:WORD_1
	s_add_u32 s28, s12, 0x1000
	global_store_dwordx2 v[94:95], v[84:85], off
	s_addc_u32 s29, s13, 0
	global_load_dwordx4 v[94:97], v[28:29], off
	global_load_dwordx4 v[98:101], v19, s[12:13]
	global_load_dwordx4 v[102:105], v19, s[28:29]
	global_load_dwordx4 v[182:185], v[28:29], off offset:1024
	global_load_dwordx4 v[186:189], v129, s[28:29]
	global_load_dwordx4 v[190:193], v19, s[12:13] offset:1024
	global_load_dwordx4 v[194:197], v[28:29], off offset:2048
	global_load_dwordx4 v[198:201], v134, s[28:29]
	global_load_dwordx4 v[202:205], v19, s[12:13] offset:2048
	global_load_dwordx4 v[206:209], v[28:29], off offset:3072
	global_load_dwordx4 v[210:213], v147, s[28:29]
	global_load_dwordx4 v[228:231], v19, s[12:13] offset:3072
	v_mov_b32_e32 v84, v72
	v_mov_b32_e32 v85, v74
	v_mov_b32_e32 v106, v73
	v_mov_b32_e32 v107, v75
	v_pk_mul_f32 v[84:85], v[84:85], v[82:83] op_sel_hi:[1,0]
	v_pk_mul_f32 v[106:107], v[106:107], v[82:83] op_sel_hi:[1,0]
	s_mov_b32 s11, 0x8ba4000
	v_readlane_b32 s26, v252, 4
	v_add_co_u32_e32 v76, vcc, s11, v76
	v_readlane_b32 s27, v252, 5
	s_nop 0
	v_addc_co_u32_e32 v77, vcc, 0, v77, vcc
	s_waitcnt vmcnt(2)
	v_mov_b32_e32 v108, v94
	v_mov_b32_e32 v109, v96
	v_mov_b32_e32 v96, v95
	s_waitcnt vmcnt(1)
	v_mov_b32_e32 v94, v98
	v_mov_b32_e32 v95, v100
	v_mov_b32_e32 v100, v99
	s_waitcnt vmcnt(0)
	v_mov_b32_e32 v98, v102
	v_mov_b32_e32 v99, v104
	v_mov_b32_e32 v104, v103
	v_pk_mul_f32 v[84:85], v[84:85], v[108:109]
	v_pk_mul_f32 v[96:97], v[106:107], v[96:97]
	v_pk_add_f32 v[98:99], v[98:99], 1.0 op_sel_hi:[1,0]
	v_pk_add_f32 v[102:103], v[104:105], 1.0 op_sel_hi:[1,0]
	v_pk_fma_f32 v[84:85], v[84:85], v[98:99], v[94:95]
	v_pk_fma_f32 v[94:95], v[96:97], v[102:103], v[100:101]
	v_mov_b32_e32 v98, v1
	v_cvt_pk_fp8_f32 v98, v84, v94
	v_and_b32_sdwa v96, v95, v236 dst_sel:DWORD dst_unused:UNUSED_PAD src0_sel:WORD_1 src1_sel:DWORD
	v_and_b32_sdwa v97, v94, v236 dst_sel:DWORD dst_unused:UNUSED_PAD src0_sel:WORD_1 src1_sel:DWORD
	v_and_b32_sdwa v86, v85, v236 dst_sel:DWORD dst_unused:UNUSED_PAD src0_sel:WORD_1 src1_sel:DWORD
	v_cvt_pk_fp8_f32 v98, v85, v95 op_sel:[0,0,1]
	v_and_b32_sdwa v88, v84, v236 dst_sel:DWORD dst_unused:UNUSED_PAD src0_sel:WORD_1 src1_sel:DWORD
	v_add3_u32 v96, v95, v96, s80
	v_add3_u32 v97, v94, v97, s80
	v_add3_u32 v88, v84, v88, s80
	v_add3_u32 v86, v85, v86, s80
	v_and_b32_e32 v96, 0xffff0000, v96
	v_and_b32_e32 v84, 0xffff0000, v97
	v_or_b32_sdwa v97, v96, v86 dst_sel:DWORD dst_unused:UNUSED_PAD src0_sel:DWORD src1_sel:WORD_1
	v_or_b32_sdwa v96, v84, v88 dst_sel:DWORD dst_unused:UNUSED_PAD src0_sel:DWORD src1_sel:WORD_1
	v_lshl_add_u64 v[84:85], s[26:27], 0, v[46:47]
	global_store_dwordx2 v[76:77], v[96:97], off offset:512
	global_store_dword v[84:85], v98, off offset:-512
	s_nop 0
	v_mov_b32_e32 v106, v78
	v_mov_b32_e32 v107, v80
	v_mov_b32_e32 v108, v79
	v_mov_b32_e32 v109, v81
	v_pk_mul_f32 v[106:107], v[106:107], v[82:83] op_sel_hi:[1,0]
	v_pk_mul_f32 v[108:109], v[108:109], v[82:83] op_sel_hi:[1,0]
	v_mov_b32_e32 v86, v1
	s_waitcnt vmcnt(2)
	v_mov_b64_e32 v[94:95], v[182:183]
	v_mov_b64_e32 v[96:97], v[184:185]
	v_mov_b32_e32 v110, v94
	v_mov_b32_e32 v111, v96
	s_waitcnt vmcnt(1)
	v_mov_b64_e32 v[98:99], v[186:187]
	v_mov_b64_e32 v[100:101], v[188:189]
	v_mov_b32_e32 v112, v98
	v_mov_b32_e32 v113, v100
	v_mov_b32_e32 v96, v95
	v_mov_b32_e32 v100, v99
	s_waitcnt vmcnt(0)
	v_mov_b64_e32 v[102:103], v[190:191]
	v_mov_b64_e32 v[104:105], v[192:193]
	v_mov_b32_e32 v114, v102
	v_mov_b32_e32 v115, v104
	v_mov_b32_e32 v104, v103
	v_pk_mul_f32 v[94:95], v[106:107], v[110:111]
	v_pk_add_f32 v[98:99], v[112:113], 1.0 op_sel_hi:[1,0]
	v_pk_mul_f32 v[96:97], v[108:109], v[96:97]
	v_pk_add_f32 v[100:101], v[100:101], 1.0 op_sel_hi:[1,0]
	v_pk_fma_f32 v[94:95], v[94:95], v[98:99], v[114:115]
	v_pk_fma_f32 v[96:97], v[96:97], v[100:101], v[104:105]
	v_and_b32_sdwa v98, v94, v236 dst_sel:DWORD dst_unused:UNUSED_PAD src0_sel:WORD_1 src1_sel:DWORD
	v_cvt_pk_fp8_f32 v86, v94, v96
	v_and_b32_sdwa v99, v97, v236 dst_sel:DWORD dst_unused:UNUSED_PAD src0_sel:WORD_1 src1_sel:DWORD
	v_and_b32_sdwa v100, v96, v236 dst_sel:DWORD dst_unused:UNUSED_PAD src0_sel:WORD_1 src1_sel:DWORD
	v_and_b32_sdwa v88, v95, v236 dst_sel:DWORD dst_unused:UNUSED_PAD src0_sel:WORD_1 src1_sel:DWORD
	v_add3_u32 v94, v94, v98, s80
	v_add3_u32 v98, v97, v99, s80
	v_add3_u32 v96, v96, v100, s80
	v_cvt_pk_fp8_f32 v86, v95, v97 op_sel:[0,0,1]
	v_add3_u32 v88, v95, v88, s80
	v_and_b32_e32 v98, 0xffff0000, v98
	v_and_b32_e32 v96, 0xffff0000, v96
	v_or_b32_sdwa v95, v98, v88 dst_sel:DWORD dst_unused:UNUSED_PAD src0_sel:DWORD src1_sel:WORD_1
	v_or_b32_sdwa v94, v96, v94 dst_sel:DWORD dst_unused:UNUSED_PAD src0_sel:DWORD src1_sel:WORD_1
	global_store_dwordx2 v[76:77], v[94:95], off offset:1024
	global_store_dword v[84:85], v86, off offset:-256
	s_nop 0
	v_mov_b32_e32 v106, v90
	v_mov_b32_e32 v107, v92
	v_mov_b32_e32 v108, v91
	v_mov_b32_e32 v109, v93
	v_pk_mul_f32 v[106:107], v[106:107], v[82:83] op_sel_hi:[1,0]
	v_pk_mul_f32 v[108:109], v[108:109], v[82:83] op_sel_hi:[1,0]
	v_mov_b32_e32 v86, v1
	s_waitcnt vmcnt(2)
	v_mov_b64_e32 v[94:95], v[194:195]
	v_mov_b64_e32 v[96:97], v[196:197]
	v_mov_b32_e32 v110, v94
	v_mov_b32_e32 v111, v96
	s_waitcnt vmcnt(1)
	v_mov_b64_e32 v[98:99], v[198:199]
	v_mov_b64_e32 v[100:101], v[200:201]
	v_mov_b32_e32 v112, v98
	v_mov_b32_e32 v113, v100
	v_mov_b32_e32 v96, v95
	v_mov_b32_e32 v100, v99
	s_waitcnt vmcnt(0)
	v_mov_b64_e32 v[102:103], v[202:203]
	v_mov_b64_e32 v[104:105], v[204:205]
	v_mov_b32_e32 v114, v102
	v_mov_b32_e32 v115, v104
	v_mov_b32_e32 v104, v103
	v_pk_mul_f32 v[94:95], v[106:107], v[110:111]
	v_pk_add_f32 v[98:99], v[112:113], 1.0 op_sel_hi:[1,0]
	v_pk_mul_f32 v[96:97], v[108:109], v[96:97]
	v_pk_add_f32 v[100:101], v[100:101], 1.0 op_sel_hi:[1,0]
	v_pk_fma_f32 v[94:95], v[94:95], v[98:99], v[114:115]
	v_pk_fma_f32 v[96:97], v[96:97], v[100:101], v[104:105]
	v_and_b32_sdwa v98, v94, v236 dst_sel:DWORD dst_unused:UNUSED_PAD src0_sel:WORD_1 src1_sel:DWORD
	v_cvt_pk_fp8_f32 v86, v94, v96
	v_and_b32_sdwa v99, v97, v236 dst_sel:DWORD dst_unused:UNUSED_PAD src0_sel:WORD_1 src1_sel:DWORD
	v_and_b32_sdwa v100, v96, v236 dst_sel:DWORD dst_unused:UNUSED_PAD src0_sel:WORD_1 src1_sel:DWORD
	v_and_b32_sdwa v88, v95, v236 dst_sel:DWORD dst_unused:UNUSED_PAD src0_sel:WORD_1 src1_sel:DWORD
	v_add3_u32 v94, v94, v98, s80
	v_add3_u32 v98, v97, v99, s80
	v_add3_u32 v96, v96, v100, s80
	v_cvt_pk_fp8_f32 v86, v95, v97 op_sel:[0,0,1]
	v_add3_u32 v88, v95, v88, s80
	v_and_b32_e32 v98, 0xffff0000, v98
	v_and_b32_e32 v96, 0xffff0000, v96
	v_or_b32_sdwa v95, v98, v88 dst_sel:DWORD dst_unused:UNUSED_PAD src0_sel:DWORD src1_sel:WORD_1
	v_or_b32_sdwa v94, v96, v94 dst_sel:DWORD dst_unused:UNUSED_PAD src0_sel:DWORD src1_sel:WORD_1
	global_store_dwordx2 v[76:77], v[94:95], off offset:1536
	global_store_dword v[84:85], v86, off
	s_nop 0
	v_mov_b32_e32 v106, v14
	v_mov_b32_e32 v107, v16
	v_mov_b32_e32 v108, v15
	v_mov_b32_e32 v109, v17
	v_pk_mul_f32 v[106:107], v[106:107], v[82:83] op_sel_hi:[1,0]
	v_pk_mul_f32 v[108:109], v[108:109], v[82:83] op_sel_hi:[1,0]
	v_mov_b32_e32 v86, v1
	s_mov_b64 s[12:13], 0
	s_waitcnt vmcnt(2)
	v_mov_b64_e32 v[94:95], v[206:207]
	v_mov_b64_e32 v[96:97], v[208:209]
	v_mov_b32_e32 v110, v94
	v_mov_b32_e32 v111, v96
	s_waitcnt vmcnt(1)
	v_mov_b64_e32 v[98:99], v[210:211]
	v_mov_b64_e32 v[100:101], v[212:213]
	v_mov_b32_e32 v112, v98
	v_mov_b32_e32 v113, v100
	v_mov_b32_e32 v96, v95
	v_mov_b32_e32 v100, v99
	s_waitcnt vmcnt(0)
	v_mov_b64_e32 v[102:103], v[228:229]
	v_mov_b64_e32 v[104:105], v[230:231]
	v_mov_b32_e32 v114, v102
	v_mov_b32_e32 v115, v104
	v_mov_b32_e32 v104, v103
	v_pk_mul_f32 v[94:95], v[106:107], v[110:111]
	v_pk_add_f32 v[98:99], v[112:113], 1.0 op_sel_hi:[1,0]
	v_pk_mul_f32 v[96:97], v[108:109], v[96:97]
	v_pk_add_f32 v[100:101], v[100:101], 1.0 op_sel_hi:[1,0]
	v_pk_fma_f32 v[94:95], v[94:95], v[98:99], v[114:115]
	v_pk_fma_f32 v[96:97], v[96:97], v[100:101], v[104:105]
	v_and_b32_sdwa v98, v94, v236 dst_sel:DWORD dst_unused:UNUSED_PAD src0_sel:WORD_1 src1_sel:DWORD
	v_cvt_pk_fp8_f32 v86, v94, v96
	v_and_b32_sdwa v99, v97, v236 dst_sel:DWORD dst_unused:UNUSED_PAD src0_sel:WORD_1 src1_sel:DWORD
	v_and_b32_sdwa v100, v96, v236 dst_sel:DWORD dst_unused:UNUSED_PAD src0_sel:WORD_1 src1_sel:DWORD
	v_and_b32_sdwa v88, v95, v236 dst_sel:DWORD dst_unused:UNUSED_PAD src0_sel:WORD_1 src1_sel:DWORD
	v_add3_u32 v94, v94, v98, s80
	v_add3_u32 v98, v97, v99, s80
	v_add3_u32 v96, v96, v100, s80
	v_cvt_pk_fp8_f32 v86, v95, v97 op_sel:[0,0,1]
	v_add3_u32 v88, v95, v88, s80
	v_and_b32_e32 v98, 0xffff0000, v98
	v_and_b32_e32 v96, 0xffff0000, v96
	v_or_b32_sdwa v95, v98, v88 dst_sel:DWORD dst_unused:UNUSED_PAD src0_sel:DWORD src1_sel:WORD_1
	v_or_b32_sdwa v94, v96, v94 dst_sel:DWORD dst_unused:UNUSED_PAD src0_sel:DWORD src1_sel:WORD_1
	global_store_dwordx2 v[76:77], v[94:95], off offset:2048
	global_store_dword v[84:85], v86, off offset:256
.LBB0_2153:
	s_andn2_b64 vcc, exec, s[12:13]
	s_cbranch_vccnz .LBB0_2155
	global_load_dwordx4 v[94:97], v[30:31], off
	global_load_dwordx4 v[170:173], v[30:31], off offset:1024
	global_load_dwordx4 v[174:177], v[30:31], off offset:2048
	global_load_dwordx4 v[178:181], v[30:31], off offset:3072
	v_pk_mul_f32 v[72:73], v[72:73], v[82:83] op_sel_hi:[1,0]
	v_pk_mul_f32 v[74:75], v[74:75], v[82:83] op_sel_hi:[1,0]
	v_lshl_add_u64 v[76:77], s[6:7], 0, v[0:1]
	v_pk_mul_f32 v[78:79], v[78:79], v[82:83] op_sel_hi:[1,0]
	v_pk_mul_f32 v[80:81], v[80:81], v[82:83] op_sel_hi:[1,0]
	v_pk_mul_f32 v[14:15], v[14:15], v[82:83] op_sel_hi:[1,0]
	v_pk_mul_f32 v[16:17], v[16:17], v[82:83] op_sel_hi:[1,0]
	s_waitcnt vmcnt(0)
	v_pk_mul_f32 v[72:73], v[72:73], v[94:95]
	v_pk_mul_f32 v[74:75], v[74:75], v[96:97]
	global_store_dwordx4 v[76:77], v[72:75], off
	s_waitcnt vmcnt(0)
	v_mov_b64_e32 v[72:73], v[170:171]
	v_mov_b64_e32 v[74:75], v[172:173]
	v_pk_mul_f32 v[72:73], v[78:79], v[72:73]
	v_pk_mul_f32 v[74:75], v[80:81], v[74:75]
	global_store_dwordx4 v[76:77], v[72:75], off offset:1024
	v_pk_mul_f32 v[78:79], v[90:91], v[82:83] op_sel_hi:[1,0]
	v_pk_mul_f32 v[80:81], v[92:93], v[82:83] op_sel_hi:[1,0]
	s_waitcnt vmcnt(0)
	v_mov_b64_e32 v[72:73], v[174:175]
	v_mov_b64_e32 v[74:75], v[176:177]
	v_pk_mul_f32 v[72:73], v[78:79], v[72:73]
	v_pk_mul_f32 v[74:75], v[80:81], v[74:75]
	global_store_dwordx4 v[76:77], v[72:75], off offset:2048
	s_waitcnt vmcnt(0)
	v_mov_b64_e32 v[72:73], v[178:179]
	v_mov_b64_e32 v[74:75], v[180:181]
	v_pk_mul_f32 v[14:15], v[14:15], v[72:73]
	v_pk_mul_f32 v[16:17], v[16:17], v[74:75]
	global_store_dwordx4 v[76:77], v[14:17], off offset:3072
.LBB0_2155:
	v_readlane_b32 s11, v254, 46
	s_cmp_ge_i32 s9, s11
	s_cbranch_scc1 .LBB0_2160
	s_ashr_i32 s11, s9, 31
	s_lshr_b32 s11, s11, 20
	s_add_i32 s11, s9, s11
	s_ashr_i32 s11, s11, 12
	s_cmp_lt_i32 s9, 0x8000
	s_cselect_b32 s9, s11, 8
	s_ashr_i32 s11, s9, 31
	s_add_u32 s12, s9, s41
	v_mul_f32_e32 v80, 0x3e000000, v10
	v_mul_f32_e32 v78, 0x3e000000, v11
	s_addc_u32 s13, s11, 0
	v_cvt_pk_f32_fp8_e32 v[10:11], v83
	v_mul_f32_e32 v76, 0x3e000000, v12
	v_mul_f32_e32 v74, 0x3e000000, v13
	s_mulk_i32 s13, 0x6000
	s_mul_hi_u32 s23, s12, 0x6000
	v_cvt_pk_f32_fp8_e32 v[12:13], v166
	s_add_i32 s23, s23, s13
	s_mulk_i32 s12, 0x6000
	v_readlane_b32 s26, v252, 4
	v_cvt_pk_f32_fp8_e32 v[14:15], v167
	v_readlane_b32 s27, v252, 5
	s_add_u32 s12, s26, s12
	v_cvt_pk_f32_fp8_e32 v[84:85], v168
	s_addc_u32 s13, s27, s23
	v_pk_fma_f32 v[10:11], v[80:81], v[10:11], 0 op_sel_hi:[0,1,0]
	s_add_u32 s12, s12, 0x105000
	v_pk_fma_f32 v[10:11], v[78:79], v[12:13], v[10:11] op_sel_hi:[0,1,1]
	s_addc_u32 s13, s13, 0
	v_pk_fma_f32 v[10:11], v[76:77], v[14:15], v[10:11] op_sel_hi:[0,1,1]
	v_pk_fma_f32 v[14:15], v[74:75], v[84:85], v[10:11] op_sel_hi:[0,1,1]
	global_load_dwordx4 v[10:13], v19, s[12:13]
	global_load_dwordx4 v[170:173], v129, s[12:13]
	global_load_dwordx4 v[174:177], v134, s[12:13]
	global_load_dwordx4 v[178:181], v147, s[12:13]
	v_cvt_pk_f32_fp8_sdwa v[16:17], v83 src0_sel:WORD_1
	v_cvt_pk_f32_fp8_sdwa v[72:73], v166 src0_sel:WORD_1
	v_cvt_pk_f32_fp8_sdwa v[82:83], v167 src0_sel:WORD_1
	v_cvt_pk_f32_fp8_sdwa v[90:91], v168 src0_sel:WORD_1
	v_lshlrev_b32_e32 v92, 16, v70
	v_and_b32_e32 v93, 0xffff0000, v70
	v_lshlrev_b32_e32 v70, 16, v71
	v_and_b32_e32 v71, 0xffff0000, v71
	v_lshlrev_b32_e32 v94, 16, v68
	v_and_b32_e32 v95, 0xffff0000, v68
	v_lshlrev_b32_e32 v96, 16, v69
	v_and_b32_e32 v97, 0xffff0000, v69
	v_lshlrev_b32_e32 v100, 16, v66
	v_and_b32_e32 v101, 0xffff0000, v66
	v_lshlrev_b32_e32 v102, 16, v67
	v_and_b32_e32 v103, 0xffff0000, v67
	v_cvt_pk_f32_fp8_sdwa v[98:99], v160 src0_sel:WORD_1
	v_cvt_pk_f32_fp8_e32 v[104:105], v157
	v_cvt_pk_f32_fp8_e32 v[106:107], v156
	v_readlane_b32 s26, v254, 44
	v_readlane_b32 s27, v254, 45
	s_waitcnt vmcnt(0)
	v_pk_fma_f32 v[14:15], v[10:11], v[14:15], v[92:93]
	v_pk_fma_f32 v[10:11], v[80:81], v[16:17], 0 op_sel_hi:[0,1,0]
	v_pk_fma_f32 v[10:11], v[78:79], v[72:73], v[10:11] op_sel_hi:[0,1,1]
	v_pk_fma_f32 v[10:11], v[76:77], v[82:83], v[10:11] op_sel_hi:[0,1,1]
	v_pk_fma_f32 v[10:11], v[74:75], v[90:91], v[10:11] op_sel_hi:[0,1,1]
	v_pk_fma_f32 v[16:17], v[10:11], v[12:13], v[70:71]
	v_cvt_pk_f32_fp8_e32 v[10:11], v87
	v_cvt_pk_f32_fp8_e32 v[12:13], v89
	v_cvt_pk_f32_fp8_sdwa v[70:71], v87 src0_sel:WORD_1
	v_cvt_pk_f32_fp8_e32 v[86:87], v164
	v_cvt_pk_f32_fp8_e32 v[90:91], v165
	v_pk_fma_f32 v[10:11], v[80:81], v[10:11], 0 op_sel_hi:[0,1,0]
	v_pk_fma_f32 v[10:11], v[78:79], v[12:13], v[10:11] op_sel_hi:[0,1,1]
	v_pk_fma_f32 v[10:11], v[76:77], v[86:87], v[10:11] op_sel_hi:[0,1,1]
	v_pk_fma_f32 v[68:69], v[74:75], v[90:91], v[10:11] op_sel_hi:[0,1,1]
	v_cvt_pk_f32_fp8_sdwa v[72:73], v89 src0_sel:WORD_1
	v_cvt_pk_f32_fp8_sdwa v[88:89], v164 src0_sel:WORD_1
	v_cvt_pk_f32_fp8_sdwa v[92:93], v165 src0_sel:WORD_1
	v_cvt_pk_f32_fp8_sdwa v[90:91], v162 src0_sel:WORD_1
	v_pk_mul_f32 v[84:85], v[14:15], v[14:15]
	v_pk_mul_f32 v[82:83], v[16:17], v[16:17]
	s_waitcnt vmcnt(0)
	v_mov_b64_e32 v[10:11], v[170:171]
	v_mov_b64_e32 v[12:13], v[172:173]
	v_pk_fma_f32 v[68:69], v[10:11], v[68:69], v[94:95]
	v_pk_fma_f32 v[10:11], v[80:81], v[70:71], 0 op_sel_hi:[0,1,0]
	v_pk_fma_f32 v[10:11], v[78:79], v[72:73], v[10:11] op_sel_hi:[0,1,1]
	v_pk_fma_f32 v[10:11], v[76:77], v[88:89], v[10:11] op_sel_hi:[0,1,1]
	v_pk_fma_f32 v[10:11], v[74:75], v[92:93], v[10:11] op_sel_hi:[0,1,1]
	v_pk_fma_f32 v[70:71], v[10:11], v[12:13], v[96:97]
	v_cvt_pk_f32_fp8_e32 v[10:11], v163
	v_cvt_pk_f32_fp8_e32 v[12:13], v162
	v_cvt_pk_f32_fp8_e32 v[92:93], v161
	v_cvt_pk_f32_fp8_e32 v[96:97], v160
	v_pk_fma_f32 v[10:11], v[80:81], v[10:11], 0 op_sel_hi:[0,1,0]
	v_pk_fma_f32 v[10:11], v[78:79], v[12:13], v[10:11] op_sel_hi:[0,1,1]
	v_pk_fma_f32 v[10:11], v[76:77], v[92:93], v[10:11] op_sel_hi:[0,1,1]
	v_pk_fma_f32 v[66:67], v[74:75], v[96:97], v[10:11] op_sel_hi:[0,1,1]
	v_cvt_pk_f32_fp8_sdwa v[72:73], v163 src0_sel:WORD_1
	v_cvt_pk_f32_fp8_sdwa v[94:95], v161 src0_sel:WORD_1
	v_cvt_pk_f32_fp8_sdwa v[96:97], v158 src0_sel:WORD_1
	v_pk_mul_f32 v[88:89], v[68:69], v[68:69]
	v_pk_mul_f32 v[86:87], v[70:71], v[70:71]
	s_waitcnt vmcnt(0)
	v_mov_b64_e32 v[10:11], v[174:175]
	v_mov_b64_e32 v[12:13], v[176:177]
	v_pk_fma_f32 v[66:67], v[10:11], v[66:67], v[100:101]
	v_pk_fma_f32 v[10:11], v[80:81], v[72:73], 0 op_sel_hi:[0,1,0]
	v_pk_fma_f32 v[10:11], v[78:79], v[90:91], v[10:11] op_sel_hi:[0,1,1]
	v_pk_fma_f32 v[10:11], v[76:77], v[94:95], v[10:11] op_sel_hi:[0,1,1]
	v_pk_fma_f32 v[10:11], v[74:75], v[98:99], v[10:11] op_sel_hi:[0,1,1]
	v_pk_fma_f32 v[72:73], v[10:11], v[12:13], v[102:103]
	v_cvt_pk_f32_fp8_e32 v[10:11], v159
	v_cvt_pk_f32_fp8_e32 v[12:13], v158
	v_cvt_pk_f32_fp8_sdwa v[94:95], v159 src0_sel:WORD_1
	v_cvt_pk_f32_fp8_sdwa v[98:99], v157 src0_sel:WORD_1
	v_pk_fma_f32 v[10:11], v[80:81], v[10:11], 0 op_sel_hi:[0,1,0]
	v_pk_fma_f32 v[10:11], v[78:79], v[12:13], v[10:11] op_sel_hi:[0,1,1]
	v_pk_fma_f32 v[10:11], v[76:77], v[104:105], v[10:11] op_sel_hi:[0,1,1]
	v_pk_fma_f32 v[104:105], v[74:75], v[106:107], v[10:11] op_sel_hi:[0,1,1]
	v_cvt_pk_f32_fp8_sdwa v[100:101], v156 src0_sel:WORD_1
	v_pk_fma_f32 v[80:81], v[80:81], v[94:95], 0 op_sel_hi:[0,1,0]
	v_pk_fma_f32 v[78:79], v[78:79], v[96:97], v[80:81] op_sel_hi:[0,1,1]
	v_pk_fma_f32 v[76:77], v[76:77], v[98:99], v[78:79] op_sel_hi:[0,1,1]
	v_pk_fma_f32 v[74:75], v[74:75], v[100:101], v[76:77] op_sel_hi:[0,1,1]
	v_add_f32_e32 v76, v88, v89
	v_add_f32_e32 v77, v84, v85
	v_lshlrev_b32_e32 v102, 16, v64
	v_and_b32_e32 v103, 0xffff0000, v64
	v_add_f32_e32 v76, v76, v86
	v_add_f32_e32 v77, v77, v82
	v_pk_mul_f32 v[92:93], v[66:67], v[66:67]
	v_lshlrev_b32_e32 v64, 16, v65
	v_and_b32_e32 v65, 0xffff0000, v65
	v_add_f32_e32 v76, v87, v76
	v_add_f32_e32 v77, v83, v77
	v_pk_mul_f32 v[90:91], v[72:73], v[72:73]
	v_add_f32_e32 v76, v77, v76
	v_add_f32_e32 v77, v92, v93
	v_add_f32_e32 v77, v77, v90
	v_add_f32_e32 v77, v91, v77
	v_add_f32_e32 v76, v76, v77
	s_mov_b32 s12, 0x800000
	s_waitcnt vmcnt(0)
	v_mov_b64_e32 v[10:11], v[178:179]
	v_mov_b64_e32 v[12:13], v[180:181]
	v_pk_fma_f32 v[10:11], v[10:11], v[104:105], v[102:103]
	v_pk_fma_f32 v[12:13], v[74:75], v[12:13], v[64:65]
	v_pk_mul_f32 v[64:65], v[10:11], v[10:11]
	v_pk_mul_f32 v[74:75], v[12:13], v[12:13]
	v_add_f32_e32 v64, v64, v65
	v_add_f32_e32 v64, v64, v74
	v_add_f32_e32 v64, v75, v64
	v_add_f32_e32 v64, v76, v64
	s_nop 1
	v_add_f32_dpp v64, v64, v64 row_ror:1 row_mask:0xf bank_mask:0xf bound_ctrl:1
	s_nop 1
	v_add_f32_dpp v64, v64, v64 row_ror:2 row_mask:0xf bank_mask:0xf bound_ctrl:1
	s_nop 1
	v_add_f32_dpp v64, v64, v64 row_ror:4 row_mask:0xf bank_mask:0xf bound_ctrl:1
	s_nop 1
	v_add_f32_dpp v64, v64, v64 row_ror:8 row_mask:0xf bank_mask:0xf bound_ctrl:1
	v_mov_b32_e32 v65, v64
	s_nop 1
	v_permlane16_swap_b32_e32 v64, v65
	v_add_f32_e32 v64, v64, v65
	v_mov_b32_e32 v65, v64
	s_nop 1
	v_permlane32_swap_b32_e32 v64, v65
	v_add_f32_e32 v64, v64, v65
	v_fmamk_f32 v64, v64, 0x3a800000, v237
	v_cmp_gt_f32_e32 vcc, s12, v64
	v_mul_f32_e32 v65, 0x4b800000, v64
	s_mov_b64 s[12:13], -1
	v_cndmask_b32_e32 v64, v64, v65, vcc
	v_rsq_f32_e32 v64, v64
	s_nop 0
	v_mul_f32_e32 v65, 0x45800000, v64
	v_cndmask_b32_e32 v64, v64, v65, vcc
	s_and_b64 vcc, exec, s[26:27]
	s_cbranch_vccz .LBB0_2158
	v_readlane_b32 s26, v252, 4
	v_and_b32_sdwa v76, v15, v236 dst_sel:DWORD dst_unused:UNUSED_PAD src0_sel:WORD_1 src1_sel:DWORD
	v_readlane_b32 s27, v252, 5
	v_and_b32_sdwa v74, v14, v236 dst_sel:DWORD dst_unused:UNUSED_PAD src0_sel:WORD_1 src1_sel:DWORD
	v_and_b32_sdwa v75, v17, v236 dst_sel:DWORD dst_unused:UNUSED_PAD src0_sel:WORD_1 src1_sel:DWORD
	v_add3_u32 v76, v15, v76, s80
	v_lshl_add_u64 v[86:87], s[26:27], 0, v[44:45]
	v_and_b32_sdwa v65, v16, v236 dst_sel:DWORD dst_unused:UNUSED_PAD src0_sel:WORD_1 src1_sel:DWORD
	v_add3_u32 v74, v14, v74, s80
	v_add3_u32 v75, v17, v75, s80
	v_and_b32_e32 v76, 0xffff0000, v76
	s_mov_b32 s12, 0x3a4000
	v_add3_u32 v65, v16, v65, s80
	v_and_b32_e32 v75, 0xffff0000, v75
	v_or_b32_sdwa v74, v76, v74 dst_sel:DWORD dst_unused:UNUSED_PAD src0_sel:DWORD src1_sel:WORD_1
	v_add_co_u32_e32 v76, vcc, s12, v86
	v_or_b32_sdwa v75, v75, v65 dst_sel:DWORD dst_unused:UNUSED_PAD src0_sel:DWORD src1_sel:WORD_1
	s_nop 0
	v_addc_co_u32_e32 v77, vcc, 0, v87, vcc
	global_store_dwordx2 v[76:77], v[74:75], off offset:512
	v_and_b32_sdwa v75, v71, v236 dst_sel:DWORD dst_unused:UNUSED_PAD src0_sel:WORD_1 src1_sel:DWORD
	v_and_b32_sdwa v78, v69, v236 dst_sel:DWORD dst_unused:UNUSED_PAD src0_sel:WORD_1 src1_sel:DWORD
	v_and_b32_sdwa v65, v70, v236 dst_sel:DWORD dst_unused:UNUSED_PAD src0_sel:WORD_1 src1_sel:DWORD
	v_and_b32_sdwa v74, v68, v236 dst_sel:DWORD dst_unused:UNUSED_PAD src0_sel:WORD_1 src1_sel:DWORD
	v_add3_u32 v75, v71, v75, s80
	v_add3_u32 v78, v69, v78, s80
	v_add3_u32 v74, v68, v74, s80
	v_add3_u32 v65, v70, v65, s80
	v_and_b32_e32 v75, 0xffff0000, v75
	v_and_b32_e32 v78, 0xffff0000, v78
	v_or_b32_sdwa v75, v75, v65 dst_sel:DWORD dst_unused:UNUSED_PAD src0_sel:DWORD src1_sel:WORD_1
	v_or_b32_sdwa v74, v78, v74 dst_sel:DWORD dst_unused:UNUSED_PAD src0_sel:DWORD src1_sel:WORD_1
	global_store_dwordx2 v[76:77], v[74:75], off offset:1024
	v_and_b32_sdwa v75, v73, v236 dst_sel:DWORD dst_unused:UNUSED_PAD src0_sel:WORD_1 src1_sel:DWORD
	v_and_b32_sdwa v78, v67, v236 dst_sel:DWORD dst_unused:UNUSED_PAD src0_sel:WORD_1 src1_sel:DWORD
	v_and_b32_sdwa v65, v72, v236 dst_sel:DWORD dst_unused:UNUSED_PAD src0_sel:WORD_1 src1_sel:DWORD
	v_and_b32_sdwa v74, v66, v236 dst_sel:DWORD dst_unused:UNUSED_PAD src0_sel:WORD_1 src1_sel:DWORD
	v_add3_u32 v75, v73, v75, s80
	v_add3_u32 v78, v67, v78, s80
	v_add3_u32 v74, v66, v74, s80
	v_add3_u32 v65, v72, v65, s80
	v_and_b32_e32 v75, 0xffff0000, v75
	v_and_b32_e32 v78, 0xffff0000, v78
	s_add_u32 s9, s9, s42
	v_or_b32_sdwa v75, v75, v65 dst_sel:DWORD dst_unused:UNUSED_PAD src0_sel:DWORD src1_sel:WORD_1
	v_or_b32_sdwa v74, v78, v74 dst_sel:DWORD dst_unused:UNUSED_PAD src0_sel:DWORD src1_sel:WORD_1
	s_addc_u32 s11, s11, 0
	global_store_dwordx2 v[76:77], v[74:75], off offset:1536
	v_and_b32_sdwa v75, v13, v236 dst_sel:DWORD dst_unused:UNUSED_PAD src0_sel:WORD_1 src1_sel:DWORD
	v_and_b32_sdwa v78, v11, v236 dst_sel:DWORD dst_unused:UNUSED_PAD src0_sel:WORD_1 src1_sel:DWORD
	s_mulk_i32 s11, 0x6000
	s_mul_hi_u32 s12, s9, 0x6000
	v_and_b32_sdwa v65, v12, v236 dst_sel:DWORD dst_unused:UNUSED_PAD src0_sel:WORD_1 src1_sel:DWORD
	v_and_b32_sdwa v74, v10, v236 dst_sel:DWORD dst_unused:UNUSED_PAD src0_sel:WORD_1 src1_sel:DWORD
	v_add3_u32 v75, v13, v75, s80
	v_add3_u32 v78, v11, v78, s80
	s_add_i32 s11, s12, s11
	s_mulk_i32 s9, 0x6000
	v_readlane_b32 s12, v253, 8
	v_add3_u32 v74, v10, v74, s80
	v_add3_u32 v65, v12, v65, s80
	v_and_b32_e32 v75, 0xffff0000, v75
	v_and_b32_e32 v78, 0xffff0000, v78
	s_add_u32 s12, s12, s9
	v_readlane_b32 s9, v253, 9
	v_or_b32_sdwa v75, v75, v65 dst_sel:DWORD dst_unused:UNUSED_PAD src0_sel:DWORD src1_sel:WORD_1
	v_or_b32_sdwa v74, v78, v74 dst_sel:DWORD dst_unused:UNUSED_PAD src0_sel:DWORD src1_sel:WORD_1
	s_addc_u32 s13, s9, s11
	global_store_dwordx2 v[76:77], v[74:75], off offset:2048
	s_add_u32 s28, s12, 0x1000
	global_load_dwordx4 v[74:77], v[28:29], off
	s_addc_u32 s29, s13, 0
	global_load_dwordx4 v[78:81], v19, s[12:13]
	global_load_dwordx4 v[82:85], v19, s[28:29]
	global_load_dwordx4 v[182:185], v[28:29], off offset:1024
	global_load_dwordx4 v[186:189], v129, s[28:29]
	global_load_dwordx4 v[190:193], v19, s[12:13] offset:1024
	global_load_dwordx4 v[194:197], v[28:29], off offset:2048
	global_load_dwordx4 v[198:201], v134, s[28:29]
	global_load_dwordx4 v[202:205], v19, s[12:13] offset:2048
	global_load_dwordx4 v[206:209], v[28:29], off offset:3072
	global_load_dwordx4 v[210:213], v147, s[28:29]
	global_load_dwordx4 v[228:231], v19, s[12:13] offset:3072
	v_mov_b32_e32 v88, v14
	v_mov_b32_e32 v89, v16
	v_mov_b32_e32 v90, v15
	v_mov_b32_e32 v91, v17
	v_pk_mul_f32 v[88:89], v[88:89], v[64:65] op_sel_hi:[1,0]
	v_pk_mul_f32 v[90:91], v[90:91], v[64:65] op_sel_hi:[1,0]
	s_mov_b32 s9, 0x8ba4000
	s_waitcnt vmcnt(2)
	v_mov_b32_e32 v92, v74
	v_mov_b32_e32 v93, v76
	v_mov_b32_e32 v76, v75
	v_pk_mul_f32 v[74:75], v[88:89], v[92:93]
	s_waitcnt vmcnt(1)
	v_mov_b32_e32 v89, v80
	v_mov_b32_e32 v80, v79
	s_waitcnt vmcnt(0)
	v_mov_b32_e32 v79, v84
	v_mov_b32_e32 v84, v83
	v_mov_b32_e32 v88, v78
	v_pk_mul_f32 v[76:77], v[90:91], v[76:77]
	v_mov_b32_e32 v78, v82
	v_pk_add_f32 v[82:83], v[84:85], 1.0 op_sel_hi:[1,0]
	v_pk_add_f32 v[78:79], v[78:79], 1.0 op_sel_hi:[1,0]
	v_pk_fma_f32 v[76:77], v[76:77], v[82:83], v[80:81]
	v_pk_fma_f32 v[78:79], v[74:75], v[78:79], v[88:89]
	v_and_b32_sdwa v75, v77, v236 dst_sel:DWORD dst_unused:UNUSED_PAD src0_sel:WORD_1 src1_sel:DWORD
	v_and_b32_sdwa v65, v79, v236 dst_sel:DWORD dst_unused:UNUSED_PAD src0_sel:WORD_1 src1_sel:DWORD
	v_add3_u32 v75, v77, v75, s80
	v_add3_u32 v65, v79, v65, s80
	v_and_b32_e32 v75, 0xffff0000, v75
	v_or_b32_sdwa v81, v75, v65 dst_sel:DWORD dst_unused:UNUSED_PAD src0_sel:DWORD src1_sel:WORD_1
	v_mov_b32_e32 v65, v1
	v_cvt_pk_fp8_f32 v65, v78, v76
	v_and_b32_sdwa v80, v76, v236 dst_sel:DWORD dst_unused:UNUSED_PAD src0_sel:WORD_1 src1_sel:DWORD
	v_and_b32_sdwa v74, v78, v236 dst_sel:DWORD dst_unused:UNUSED_PAD src0_sel:WORD_1 src1_sel:DWORD
	v_add3_u32 v80, v76, v80, s80
	v_add3_u32 v74, v78, v74, s80
	v_and_b32_e32 v80, 0xffff0000, v80
	v_or_b32_sdwa v80, v80, v74 dst_sel:DWORD dst_unused:UNUSED_PAD src0_sel:DWORD src1_sel:WORD_1
	v_add_co_u32_e32 v74, vcc, s9, v86
	v_cvt_pk_fp8_f32 v65, v79, v77 op_sel:[0,0,1]
	s_nop 0
	v_addc_co_u32_e32 v75, vcc, 0, v87, vcc
	v_lshl_add_u64 v[76:77], s[26:27], 0, v[42:43]
	s_mov_b32 s9, 0x43b44000
	v_add_co_u32_e32 v76, vcc, s9, v76
	global_store_dwordx2 v[74:75], v[80:81], off offset:512
	s_nop 0
	v_addc_co_u32_e32 v77, vcc, 0, v77, vcc
	global_store_dword v[76:77], v65, off offset:512
	v_mov_b32_e32 v90, v68
	v_mov_b32_e32 v91, v70
	v_mov_b32_e32 v92, v69
	v_mov_b32_e32 v93, v71
	v_mov_b32_e32 v65, v1
	v_pk_mul_f32 v[90:91], v[90:91], v[64:65] op_sel_hi:[1,0]
	v_pk_mul_f32 v[92:93], v[92:93], v[64:65] op_sel_hi:[1,0]
	s_waitcnt vmcnt(2)
	v_mov_b64_e32 v[78:79], v[182:183]
	v_mov_b64_e32 v[80:81], v[184:185]
	v_mov_b32_e32 v94, v78
	v_mov_b32_e32 v95, v80
	s_waitcnt vmcnt(1)
	v_mov_b64_e32 v[82:83], v[186:187]
	v_mov_b64_e32 v[84:85], v[188:189]
	v_mov_b32_e32 v96, v82
	v_mov_b32_e32 v97, v84
	v_mov_b32_e32 v80, v79
	v_mov_b32_e32 v84, v83
	s_waitcnt vmcnt(0)
	v_mov_b64_e32 v[86:87], v[190:191]
	v_mov_b64_e32 v[88:89], v[192:193]
	v_mov_b32_e32 v98, v86
	v_mov_b32_e32 v99, v88
	v_mov_b32_e32 v88, v87
	v_pk_mul_f32 v[78:79], v[90:91], v[94:95]
	v_pk_add_f32 v[82:83], v[96:97], 1.0 op_sel_hi:[1,0]
	v_pk_mul_f32 v[80:81], v[92:93], v[80:81]
	v_pk_add_f32 v[84:85], v[84:85], 1.0 op_sel_hi:[1,0]
	v_pk_fma_f32 v[78:79], v[78:79], v[82:83], v[98:99]
	v_pk_fma_f32 v[80:81], v[80:81], v[84:85], v[88:89]
	v_and_b32_sdwa v83, v78, v236 dst_sel:DWORD dst_unused:UNUSED_PAD src0_sel:WORD_1 src1_sel:DWORD
	v_cvt_pk_fp8_f32 v65, v78, v80
	v_and_b32_sdwa v84, v81, v236 dst_sel:DWORD dst_unused:UNUSED_PAD src0_sel:WORD_1 src1_sel:DWORD
	v_and_b32_sdwa v85, v80, v236 dst_sel:DWORD dst_unused:UNUSED_PAD src0_sel:WORD_1 src1_sel:DWORD
	v_and_b32_sdwa v82, v79, v236 dst_sel:DWORD dst_unused:UNUSED_PAD src0_sel:WORD_1 src1_sel:DWORD
	v_add3_u32 v78, v78, v83, s80
	v_add3_u32 v83, v81, v84, s80
	v_add3_u32 v80, v80, v85, s80
	v_cvt_pk_fp8_f32 v65, v79, v81 op_sel:[0,0,1]
	v_add3_u32 v82, v79, v82, s80
	v_and_b32_e32 v83, 0xffff0000, v83
	v_and_b32_e32 v80, 0xffff0000, v80
	v_or_b32_sdwa v79, v83, v82 dst_sel:DWORD dst_unused:UNUSED_PAD src0_sel:DWORD src1_sel:WORD_1
	v_or_b32_sdwa v78, v80, v78 dst_sel:DWORD dst_unused:UNUSED_PAD src0_sel:DWORD src1_sel:WORD_1
	global_store_dwordx2 v[74:75], v[78:79], off offset:1024
	global_store_dword v[76:77], v65, off offset:768
	s_nop 0
	v_mov_b32_e32 v90, v66
	v_mov_b32_e32 v91, v72
	v_mov_b32_e32 v92, v67
	v_mov_b32_e32 v93, v73
	v_mov_b32_e32 v65, v1
	v_pk_mul_f32 v[90:91], v[90:91], v[64:65] op_sel_hi:[1,0]
	v_pk_mul_f32 v[92:93], v[92:93], v[64:65] op_sel_hi:[1,0]
	s_waitcnt vmcnt(2)
	v_mov_b64_e32 v[78:79], v[194:195]
	v_mov_b64_e32 v[80:81], v[196:197]
	v_mov_b32_e32 v94, v78
	v_mov_b32_e32 v95, v80
	s_waitcnt vmcnt(1)
	v_mov_b64_e32 v[82:83], v[198:199]
	v_mov_b64_e32 v[84:85], v[200:201]
	v_mov_b32_e32 v96, v82
	v_mov_b32_e32 v97, v84
	v_mov_b32_e32 v80, v79
	v_mov_b32_e32 v84, v83
	s_waitcnt vmcnt(0)
	v_mov_b64_e32 v[86:87], v[202:203]
	v_mov_b64_e32 v[88:89], v[204:205]
	v_mov_b32_e32 v98, v86
	v_mov_b32_e32 v99, v88
	v_mov_b32_e32 v88, v87
	v_pk_mul_f32 v[78:79], v[90:91], v[94:95]
	v_pk_add_f32 v[82:83], v[96:97], 1.0 op_sel_hi:[1,0]
	v_pk_mul_f32 v[80:81], v[92:93], v[80:81]
	v_pk_add_f32 v[84:85], v[84:85], 1.0 op_sel_hi:[1,0]
	v_pk_fma_f32 v[78:79], v[78:79], v[82:83], v[98:99]
	v_pk_fma_f32 v[80:81], v[80:81], v[84:85], v[88:89]
	v_and_b32_sdwa v83, v78, v236 dst_sel:DWORD dst_unused:UNUSED_PAD src0_sel:WORD_1 src1_sel:DWORD
	v_cvt_pk_fp8_f32 v65, v78, v80
	v_and_b32_sdwa v84, v81, v236 dst_sel:DWORD dst_unused:UNUSED_PAD src0_sel:WORD_1 src1_sel:DWORD
	v_and_b32_sdwa v85, v80, v236 dst_sel:DWORD dst_unused:UNUSED_PAD src0_sel:WORD_1 src1_sel:DWORD
	v_and_b32_sdwa v82, v79, v236 dst_sel:DWORD dst_unused:UNUSED_PAD src0_sel:WORD_1 src1_sel:DWORD
	v_add3_u32 v78, v78, v83, s80
	v_add3_u32 v83, v81, v84, s80
	v_add3_u32 v80, v80, v85, s80
	v_cvt_pk_fp8_f32 v65, v79, v81 op_sel:[0,0,1]
	v_add3_u32 v82, v79, v82, s80
	v_and_b32_e32 v83, 0xffff0000, v83
	v_and_b32_e32 v80, 0xffff0000, v80
	v_or_b32_sdwa v79, v83, v82 dst_sel:DWORD dst_unused:UNUSED_PAD src0_sel:DWORD src1_sel:WORD_1
	v_or_b32_sdwa v78, v80, v78 dst_sel:DWORD dst_unused:UNUSED_PAD src0_sel:DWORD src1_sel:WORD_1
	global_store_dwordx2 v[74:75], v[78:79], off offset:1536
	global_store_dword v[76:77], v65, off offset:1024
	s_nop 0
	v_mov_b32_e32 v90, v10
	v_mov_b32_e32 v91, v12
	v_mov_b32_e32 v92, v11
	v_mov_b32_e32 v93, v13
	v_mov_b32_e32 v65, v1
	v_pk_mul_f32 v[90:91], v[90:91], v[64:65] op_sel_hi:[1,0]
	v_pk_mul_f32 v[92:93], v[92:93], v[64:65] op_sel_hi:[1,0]
	s_mov_b64 s[12:13], 0
	s_waitcnt vmcnt(2)
	v_mov_b64_e32 v[78:79], v[206:207]
	v_mov_b64_e32 v[80:81], v[208:209]
	v_mov_b32_e32 v94, v78
	v_mov_b32_e32 v95, v80
	s_waitcnt vmcnt(1)
	v_mov_b64_e32 v[82:83], v[210:211]
	v_mov_b64_e32 v[84:85], v[212:213]
	v_mov_b32_e32 v96, v82
	v_mov_b32_e32 v97, v84
	v_mov_b32_e32 v80, v79
	v_mov_b32_e32 v84, v83
	s_waitcnt vmcnt(0)
	v_mov_b64_e32 v[86:87], v[228:229]
	v_mov_b64_e32 v[88:89], v[230:231]
	v_mov_b32_e32 v98, v86
	v_mov_b32_e32 v99, v88
	v_mov_b32_e32 v88, v87
	v_pk_mul_f32 v[78:79], v[90:91], v[94:95]
	v_pk_add_f32 v[82:83], v[96:97], 1.0 op_sel_hi:[1,0]
	v_pk_mul_f32 v[80:81], v[92:93], v[80:81]
	v_pk_add_f32 v[84:85], v[84:85], 1.0 op_sel_hi:[1,0]
	v_pk_fma_f32 v[78:79], v[78:79], v[82:83], v[98:99]
	v_pk_fma_f32 v[80:81], v[80:81], v[84:85], v[88:89]
	v_and_b32_sdwa v83, v78, v236 dst_sel:DWORD dst_unused:UNUSED_PAD src0_sel:WORD_1 src1_sel:DWORD
	v_cvt_pk_fp8_f32 v65, v78, v80
	v_and_b32_sdwa v84, v81, v236 dst_sel:DWORD dst_unused:UNUSED_PAD src0_sel:WORD_1 src1_sel:DWORD
	v_and_b32_sdwa v85, v80, v236 dst_sel:DWORD dst_unused:UNUSED_PAD src0_sel:WORD_1 src1_sel:DWORD
	v_and_b32_sdwa v82, v79, v236 dst_sel:DWORD dst_unused:UNUSED_PAD src0_sel:WORD_1 src1_sel:DWORD
	v_add3_u32 v78, v78, v83, s80
	v_add3_u32 v83, v81, v84, s80
	v_add3_u32 v80, v80, v85, s80
	v_cvt_pk_fp8_f32 v65, v79, v81 op_sel:[0,0,1]
	v_add3_u32 v82, v79, v82, s80
	v_and_b32_e32 v83, 0xffff0000, v83
	v_and_b32_e32 v80, 0xffff0000, v80
	v_or_b32_sdwa v79, v83, v82 dst_sel:DWORD dst_unused:UNUSED_PAD src0_sel:DWORD src1_sel:WORD_1
	v_or_b32_sdwa v78, v80, v78 dst_sel:DWORD dst_unused:UNUSED_PAD src0_sel:DWORD src1_sel:WORD_1
	global_store_dwordx2 v[74:75], v[78:79], off offset:2048
	global_store_dword v[76:77], v65, off offset:1280
.LBB0_2158:
	s_andn2_b64 vcc, exec, s[12:13]
	s_cbranch_vccnz .LBB0_2160
	global_load_dwordx4 v[74:77], v[30:31], off
	global_load_dwordx4 v[170:173], v[30:31], off offset:1024
	global_load_dwordx4 v[174:177], v[30:31], off offset:2048
	global_load_dwordx4 v[178:181], v[30:31], off offset:3072
	v_pk_mul_f32 v[14:15], v[14:15], v[64:65] op_sel_hi:[1,0]
	v_pk_mul_f32 v[16:17], v[16:17], v[64:65] op_sel_hi:[1,0]
	v_lshl_add_u64 v[78:79], s[0:1], 0, v[0:1]
	v_pk_mul_f32 v[68:69], v[68:69], v[64:65] op_sel_hi:[1,0]
	v_pk_mul_f32 v[70:71], v[70:71], v[64:65] op_sel_hi:[1,0]
	v_pk_mul_f32 v[66:67], v[66:67], v[64:65] op_sel_hi:[1,0]
	v_pk_mul_f32 v[10:11], v[10:11], v[64:65] op_sel_hi:[1,0]
	v_pk_mul_f32 v[12:13], v[12:13], v[64:65] op_sel_hi:[1,0]
	s_waitcnt vmcnt(0)
	v_pk_mul_f32 v[14:15], v[14:15], v[74:75]
	v_pk_mul_f32 v[16:17], v[16:17], v[76:77]
	global_store_dwordx4 v[78:79], v[14:17], off
	s_waitcnt vmcnt(0)
	v_mov_b64_e32 v[14:15], v[170:171]
	v_mov_b64_e32 v[16:17], v[172:173]
	v_pk_mul_f32 v[14:15], v[68:69], v[14:15]
	v_pk_mul_f32 v[16:17], v[70:71], v[16:17]
	global_store_dwordx4 v[78:79], v[14:17], off offset:1024
	v_pk_mul_f32 v[68:69], v[72:73], v[64:65] op_sel_hi:[1,0]
	s_waitcnt vmcnt(0)
	v_mov_b64_e32 v[14:15], v[174:175]
	v_mov_b64_e32 v[16:17], v[176:177]
	v_pk_mul_f32 v[14:15], v[66:67], v[14:15]
	v_pk_mul_f32 v[16:17], v[68:69], v[16:17]
	global_store_dwordx4 v[78:79], v[14:17], off offset:2048
	s_waitcnt vmcnt(0)
	v_mov_b64_e32 v[14:15], v[178:179]
	v_mov_b64_e32 v[16:17], v[180:181]
	v_pk_mul_f32 v[10:11], v[10:11], v[14:15]
	v_pk_mul_f32 v[12:13], v[12:13], v[16:17]
	global_store_dwordx4 v[78:79], v[10:13], off offset:3072
.LBB0_2160:
	v_readlane_b32 s9, v254, 46
	s_cmp_ge_i32 s10, s9
	s_cbranch_scc1 .LBB0_2165
	s_ashr_i32 s11, s10, 31
	s_lshr_b32 s9, s11, 20
	s_add_i32 s9, s10, s9
	s_lshl_b64 s[12:13], s[10:11], 10
	s_ashr_i32 s9, s9, 12
	s_cmp_lt_i32 s10, 0x8000
	s_cselect_b32 s9, s9, 8
	s_ashr_i32 s23, s9, 31
	s_add_u32 s10, s9, s41
	v_mul_f32_e32 v70, 0x3e000000, v6
	v_mul_f32_e32 v68, 0x3e000000, v7
	s_addc_u32 s11, s23, 0
	v_cvt_pk_f32_fp8_e32 v[6:7], v152
	v_mul_f32_e32 v66, 0x3e000000, v8
	v_mul_f32_e32 v64, 0x3e000000, v9
	s_mulk_i32 s11, 0x6000
	s_mul_hi_u32 s26, s10, 0x6000
	v_cvt_pk_f32_fp8_e32 v[8:9], v153
	s_add_i32 s26, s26, s11
	s_mulk_i32 s10, 0x6000
	v_readlane_b32 s28, v252, 4
	v_cvt_pk_f32_fp8_e32 v[10:11], v154
	v_readlane_b32 s29, v252, 5
	s_add_u32 s10, s28, s10
	v_cvt_pk_f32_fp8_e32 v[72:73], v155
	s_addc_u32 s11, s29, s26
	v_pk_fma_f32 v[6:7], v[70:71], v[6:7], 0 op_sel_hi:[0,1,0]
	s_add_u32 s10, s10, 0x105000
	v_pk_fma_f32 v[6:7], v[68:69], v[8:9], v[6:7] op_sel_hi:[0,1,1]
	s_addc_u32 s11, s11, 0
	v_pk_fma_f32 v[6:7], v[66:67], v[10:11], v[6:7] op_sel_hi:[0,1,1]
	v_pk_fma_f32 v[10:11], v[64:65], v[72:73], v[6:7] op_sel_hi:[0,1,1]
	global_load_dwordx4 v[6:9], v19, s[10:11]
	global_load_dwordx4 v[170:173], v129, s[10:11]
	global_load_dwordx4 v[174:177], v134, s[10:11]
	global_load_dwordx4 v[178:181], v147, s[10:11]
	v_cvt_pk_f32_fp8_sdwa v[12:13], v152 src0_sel:WORD_1
	v_cvt_pk_f32_fp8_sdwa v[14:15], v153 src0_sel:WORD_1
	v_cvt_pk_f32_fp8_sdwa v[16:17], v154 src0_sel:WORD_1
	v_cvt_pk_f32_fp8_sdwa v[74:75], v155 src0_sel:WORD_1
	v_lshlrev_b32_e32 v76, 16, v62
	v_and_b32_e32 v77, 0xffff0000, v62
	v_lshlrev_b32_e32 v62, 16, v63
	v_and_b32_e32 v63, 0xffff0000, v63
	v_cvt_pk_f32_fp8_e32 v[78:79], v151
	v_cvt_pk_f32_fp8_sdwa v[80:81], v151 src0_sel:WORD_1
	v_lshlrev_b32_e32 v82, 16, v60
	v_and_b32_e32 v83, 0xffff0000, v60
	v_lshlrev_b32_e32 v60, 16, v61
	v_and_b32_e32 v61, 0xffff0000, v61
	v_cvt_pk_f32_fp8_e32 v[84:85], v143
	v_lshlrev_b32_e32 v88, 16, v58
	v_and_b32_e32 v89, 0xffff0000, v58
	v_lshlrev_b32_e32 v90, 16, v59
	v_and_b32_e32 v91, 0xffff0000, v59
	v_cvt_pk_f32_fp8_sdwa v[86:87], v143 src0_sel:WORD_1
	v_cvt_pk_f32_fp8_e32 v[92:93], v140
	v_cvt_pk_f32_fp8_e32 v[94:95], v139
	v_readlane_b32 s26, v254, 44
	v_readlane_b32 s27, v254, 45
	s_waitcnt vmcnt(0)
	v_pk_fma_f32 v[10:11], v[6:7], v[10:11], v[76:77]
	v_pk_fma_f32 v[6:7], v[70:71], v[12:13], 0 op_sel_hi:[0,1,0]
	v_pk_fma_f32 v[6:7], v[68:69], v[14:15], v[6:7] op_sel_hi:[0,1,1]
	v_pk_fma_f32 v[6:7], v[66:67], v[16:17], v[6:7] op_sel_hi:[0,1,1]
	v_pk_fma_f32 v[6:7], v[64:65], v[74:75], v[6:7] op_sel_hi:[0,1,1]
	v_pk_fma_f32 v[12:13], v[6:7], v[8:9], v[62:63]
	v_cvt_pk_f32_fp8_e32 v[6:7], v148
	v_cvt_pk_f32_fp8_e32 v[8:9], v149
	v_cvt_pk_f32_fp8_e32 v[14:15], v150
	v_cvt_pk_f32_fp8_sdwa v[16:17], v148 src0_sel:WORD_1
	v_pk_fma_f32 v[6:7], v[70:71], v[6:7], 0 op_sel_hi:[0,1,0]
	v_pk_fma_f32 v[6:7], v[68:69], v[8:9], v[6:7] op_sel_hi:[0,1,1]
	v_pk_fma_f32 v[6:7], v[66:67], v[14:15], v[6:7] op_sel_hi:[0,1,1]
	v_pk_fma_f32 v[14:15], v[64:65], v[78:79], v[6:7] op_sel_hi:[0,1,1]
	v_cvt_pk_f32_fp8_sdwa v[74:75], v149 src0_sel:WORD_1
	v_cvt_pk_f32_fp8_sdwa v[76:77], v150 src0_sel:WORD_1
	v_cvt_pk_f32_fp8_sdwa v[78:79], v145 src0_sel:WORD_1
	v_pk_mul_f32 v[72:73], v[10:11], v[10:11]
	v_pk_mul_f32 v[62:63], v[12:13], v[12:13]
	s_waitcnt vmcnt(0)
	v_mov_b64_e32 v[6:7], v[170:171]
	v_mov_b64_e32 v[8:9], v[172:173]
	v_pk_fma_f32 v[14:15], v[6:7], v[14:15], v[82:83]
	v_pk_fma_f32 v[6:7], v[70:71], v[16:17], 0 op_sel_hi:[0,1,0]
	v_pk_fma_f32 v[6:7], v[68:69], v[74:75], v[6:7] op_sel_hi:[0,1,1]
	v_pk_fma_f32 v[6:7], v[66:67], v[76:77], v[6:7] op_sel_hi:[0,1,1]
	v_pk_fma_f32 v[6:7], v[64:65], v[80:81], v[6:7] op_sel_hi:[0,1,1]
	v_pk_fma_f32 v[16:17], v[6:7], v[8:9], v[60:61]
	v_cvt_pk_f32_fp8_e32 v[6:7], v146
	v_cvt_pk_f32_fp8_e32 v[8:9], v145
	v_cvt_pk_f32_fp8_e32 v[80:81], v144
	v_cvt_pk_f32_fp8_sdwa v[60:61], v146 src0_sel:WORD_1
	v_pk_fma_f32 v[6:7], v[70:71], v[6:7], 0 op_sel_hi:[0,1,0]
	v_pk_fma_f32 v[6:7], v[68:69], v[8:9], v[6:7] op_sel_hi:[0,1,1]
	v_pk_fma_f32 v[6:7], v[66:67], v[80:81], v[6:7] op_sel_hi:[0,1,1]
	v_pk_fma_f32 v[58:59], v[64:65], v[84:85], v[6:7] op_sel_hi:[0,1,1]
	v_cvt_pk_f32_fp8_sdwa v[82:83], v144 src0_sel:WORD_1
	v_cvt_pk_f32_fp8_sdwa v[84:85], v141 src0_sel:WORD_1
	v_pk_mul_f32 v[76:77], v[14:15], v[14:15]
	v_pk_mul_f32 v[74:75], v[16:17], v[16:17]
	s_waitcnt vmcnt(0)
	v_mov_b64_e32 v[6:7], v[174:175]
	v_mov_b64_e32 v[8:9], v[176:177]
	v_pk_fma_f32 v[58:59], v[6:7], v[58:59], v[88:89]
	v_pk_fma_f32 v[6:7], v[70:71], v[60:61], 0 op_sel_hi:[0,1,0]
	v_pk_fma_f32 v[6:7], v[68:69], v[78:79], v[6:7] op_sel_hi:[0,1,1]
	v_pk_fma_f32 v[6:7], v[66:67], v[82:83], v[6:7] op_sel_hi:[0,1,1]
	v_pk_fma_f32 v[6:7], v[64:65], v[86:87], v[6:7] op_sel_hi:[0,1,1]
	v_pk_fma_f32 v[60:61], v[6:7], v[8:9], v[90:91]
	v_cvt_pk_f32_fp8_e32 v[6:7], v142
	v_cvt_pk_f32_fp8_e32 v[8:9], v141
	v_cvt_pk_f32_fp8_sdwa v[82:83], v142 src0_sel:WORD_1
	v_cvt_pk_f32_fp8_sdwa v[86:87], v140 src0_sel:WORD_1
	v_pk_fma_f32 v[6:7], v[70:71], v[6:7], 0 op_sel_hi:[0,1,0]
	v_pk_fma_f32 v[6:7], v[68:69], v[8:9], v[6:7] op_sel_hi:[0,1,1]
	v_pk_fma_f32 v[6:7], v[66:67], v[92:93], v[6:7] op_sel_hi:[0,1,1]
	v_pk_fma_f32 v[92:93], v[64:65], v[94:95], v[6:7] op_sel_hi:[0,1,1]
	v_cvt_pk_f32_fp8_sdwa v[88:89], v139 src0_sel:WORD_1
	v_pk_fma_f32 v[70:71], v[70:71], v[82:83], 0 op_sel_hi:[0,1,0]
	v_pk_fma_f32 v[68:69], v[68:69], v[84:85], v[70:71] op_sel_hi:[0,1,1]
	v_pk_fma_f32 v[66:67], v[66:67], v[86:87], v[68:69] op_sel_hi:[0,1,1]
	v_lshlrev_b32_e32 v90, 16, v56
	v_and_b32_e32 v91, 0xffff0000, v56
	v_pk_fma_f32 v[64:65], v[64:65], v[88:89], v[66:67] op_sel_hi:[0,1,1]
	v_add_f32_e32 v67, v72, v73
	v_pk_mul_f32 v[80:81], v[58:59], v[58:59]
	v_lshlrev_b32_e32 v56, 16, v57
	v_and_b32_e32 v57, 0xffff0000, v57
	v_add_f32_e32 v66, v76, v77
	v_add_f32_e32 v62, v67, v62
	v_pk_mul_f32 v[78:79], v[60:61], v[60:61]
	v_add_f32_e32 v66, v66, v74
	v_add_f32_e32 v62, v63, v62
	v_add_f32_e32 v63, v80, v81
	v_add_f32_e32 v66, v75, v66
	v_add_f32_e32 v63, v63, v78
	v_add_f32_e32 v62, v62, v66
	v_add_f32_e32 v63, v79, v63
	v_add_f32_e32 v62, v62, v63
	s_mov_b32 s10, 0x800000
	s_waitcnt vmcnt(0)
	v_mov_b64_e32 v[6:7], v[178:179]
	v_mov_b64_e32 v[8:9], v[180:181]
	v_pk_fma_f32 v[6:7], v[6:7], v[92:93], v[90:91]
	v_pk_fma_f32 v[8:9], v[64:65], v[8:9], v[56:57]
	v_pk_mul_f32 v[56:57], v[6:7], v[6:7]
	v_pk_mul_f32 v[64:65], v[8:9], v[8:9]
	v_add_f32_e32 v56, v56, v57
	v_add_f32_e32 v56, v56, v64
	v_add_f32_e32 v56, v65, v56
	v_add_f32_e32 v56, v62, v56
	s_nop 1
	v_add_f32_dpp v56, v56, v56 row_ror:1 row_mask:0xf bank_mask:0xf bound_ctrl:1
	s_nop 1
	v_add_f32_dpp v56, v56, v56 row_ror:2 row_mask:0xf bank_mask:0xf bound_ctrl:1
	s_nop 1
	v_add_f32_dpp v56, v56, v56 row_ror:4 row_mask:0xf bank_mask:0xf bound_ctrl:1
	s_nop 1
	v_add_f32_dpp v56, v56, v56 row_ror:8 row_mask:0xf bank_mask:0xf bound_ctrl:1
	v_mov_b32_e32 v57, v56
	s_nop 1
	v_permlane16_swap_b32_e32 v56, v57
	v_add_f32_e32 v56, v56, v57
	v_mov_b32_e32 v57, v56
	s_nop 1
	v_permlane32_swap_b32_e32 v56, v57
	v_add_f32_e32 v56, v56, v57
	v_fmamk_f32 v56, v56, 0x3a800000, v237
	v_cmp_gt_f32_e32 vcc, s10, v56
	v_mul_f32_e32 v57, 0x4b800000, v56
	s_mov_b64 s[10:11], -1
	v_cndmask_b32_e32 v56, v56, v57, vcc
	v_rsq_f32_e32 v56, v56
	s_nop 0
	v_mul_f32_e32 v57, 0x45800000, v56
	v_cndmask_b32_e32 v56, v56, v57, vcc
	s_and_b64 vcc, exec, s[26:27]
	s_cbranch_vccz .LBB0_2163
	v_and_b32_sdwa v65, v13, v236 dst_sel:DWORD dst_unused:UNUSED_PAD src0_sel:WORD_1 src1_sel:DWORD
	v_and_b32_sdwa v66, v11, v236 dst_sel:DWORD dst_unused:UNUSED_PAD src0_sel:WORD_1 src1_sel:DWORD
	v_and_b32_sdwa v57, v12, v236 dst_sel:DWORD dst_unused:UNUSED_PAD src0_sel:WORD_1 src1_sel:DWORD
	v_and_b32_sdwa v64, v10, v236 dst_sel:DWORD dst_unused:UNUSED_PAD src0_sel:WORD_1 src1_sel:DWORD
	v_add3_u32 v65, v13, v65, s80
	v_add3_u32 v66, v11, v66, s80
	s_lshl_b64 s[30:31], s[12:13], 1
	v_add3_u32 v64, v10, v64, s80
	v_add3_u32 v57, v12, v57, s80
	v_and_b32_e32 v65, 0xffff0000, v65
	v_and_b32_e32 v66, 0xffff0000, v66
	v_lshl_add_u64 v[62:63], v[32:33], 0, s[30:31]
	v_or_b32_sdwa v65, v65, v57 dst_sel:DWORD dst_unused:UNUSED_PAD src0_sel:DWORD src1_sel:WORD_1
	v_or_b32_sdwa v64, v66, v64 dst_sel:DWORD dst_unused:UNUSED_PAD src0_sel:DWORD src1_sel:WORD_1
	global_store_dwordx2 v[62:63], v[64:65], off
	v_and_b32_sdwa v65, v17, v236 dst_sel:DWORD dst_unused:UNUSED_PAD src0_sel:WORD_1 src1_sel:DWORD
	v_and_b32_sdwa v66, v15, v236 dst_sel:DWORD dst_unused:UNUSED_PAD src0_sel:WORD_1 src1_sel:DWORD
	v_and_b32_sdwa v57, v16, v236 dst_sel:DWORD dst_unused:UNUSED_PAD src0_sel:WORD_1 src1_sel:DWORD
	v_and_b32_sdwa v64, v14, v236 dst_sel:DWORD dst_unused:UNUSED_PAD src0_sel:WORD_1 src1_sel:DWORD
	v_add3_u32 v65, v17, v65, s80
	v_add3_u32 v66, v15, v66, s80
	v_add3_u32 v64, v14, v64, s80
	v_add3_u32 v57, v16, v57, s80
	v_and_b32_e32 v65, 0xffff0000, v65
	v_and_b32_e32 v66, 0xffff0000, v66
	v_or_b32_sdwa v65, v65, v57 dst_sel:DWORD dst_unused:UNUSED_PAD src0_sel:DWORD src1_sel:WORD_1
	v_or_b32_sdwa v64, v66, v64 dst_sel:DWORD dst_unused:UNUSED_PAD src0_sel:DWORD src1_sel:WORD_1
	global_store_dwordx2 v[62:63], v[64:65], off offset:512
	v_and_b32_sdwa v65, v61, v236 dst_sel:DWORD dst_unused:UNUSED_PAD src0_sel:WORD_1 src1_sel:DWORD
	v_and_b32_sdwa v66, v59, v236 dst_sel:DWORD dst_unused:UNUSED_PAD src0_sel:WORD_1 src1_sel:DWORD
	v_and_b32_sdwa v57, v60, v236 dst_sel:DWORD dst_unused:UNUSED_PAD src0_sel:WORD_1 src1_sel:DWORD
	v_and_b32_sdwa v64, v58, v236 dst_sel:DWORD dst_unused:UNUSED_PAD src0_sel:WORD_1 src1_sel:DWORD
	v_add3_u32 v65, v61, v65, s80
	v_add3_u32 v66, v59, v66, s80
	v_add3_u32 v64, v58, v64, s80
	v_add3_u32 v57, v60, v57, s80
	v_and_b32_e32 v65, 0xffff0000, v65
	v_and_b32_e32 v66, 0xffff0000, v66
	s_add_u32 s9, s9, s42
	v_or_b32_sdwa v65, v65, v57 dst_sel:DWORD dst_unused:UNUSED_PAD src0_sel:DWORD src1_sel:WORD_1
	v_or_b32_sdwa v64, v66, v64 dst_sel:DWORD dst_unused:UNUSED_PAD src0_sel:DWORD src1_sel:WORD_1
	s_addc_u32 s10, s23, 0
	global_store_dwordx2 v[62:63], v[64:65], off offset:1024
	v_and_b32_sdwa v65, v9, v236 dst_sel:DWORD dst_unused:UNUSED_PAD src0_sel:WORD_1 src1_sel:DWORD
	v_and_b32_sdwa v66, v7, v236 dst_sel:DWORD dst_unused:UNUSED_PAD src0_sel:WORD_1 src1_sel:DWORD
	s_mulk_i32 s10, 0x6000
	s_mul_hi_u32 s11, s9, 0x6000
	v_and_b32_sdwa v57, v8, v236 dst_sel:DWORD dst_unused:UNUSED_PAD src0_sel:WORD_1 src1_sel:DWORD
	v_and_b32_sdwa v64, v6, v236 dst_sel:DWORD dst_unused:UNUSED_PAD src0_sel:WORD_1 src1_sel:DWORD
	v_add3_u32 v65, v9, v65, s80
	v_add3_u32 v66, v7, v66, s80
	s_add_i32 s11, s11, s10
	s_mulk_i32 s9, 0x6000
	v_readlane_b32 s10, v253, 8
	v_add3_u32 v64, v6, v64, s80
	v_add3_u32 v57, v8, v57, s80
	v_and_b32_e32 v65, 0xffff0000, v65
	v_and_b32_e32 v66, 0xffff0000, v66
	s_add_u32 s10, s10, s9
	v_readlane_b32 s9, v253, 9
	v_or_b32_sdwa v65, v65, v57 dst_sel:DWORD dst_unused:UNUSED_PAD src0_sel:DWORD src1_sel:WORD_1
	v_or_b32_sdwa v64, v66, v64 dst_sel:DWORD dst_unused:UNUSED_PAD src0_sel:DWORD src1_sel:WORD_1
	s_addc_u32 s11, s9, s11
	global_store_dwordx2 v[62:63], v[64:65], off offset:1536
	s_add_u32 s28, s10, 0x1000
	global_load_dwordx4 v[64:67], v[28:29], off
	s_addc_u32 s29, s11, 0
	global_load_dwordx4 v[68:71], v19, s[10:11]
	global_load_dwordx4 v[72:75], v19, s[28:29]
	global_load_dwordx4 v[182:185], v[28:29], off offset:1024
	global_load_dwordx4 v[186:189], v129, s[28:29]
	global_load_dwordx4 v[190:193], v19, s[10:11] offset:1024
	global_load_dwordx4 v[194:197], v[28:29], off offset:2048
	global_load_dwordx4 v[198:201], v134, s[28:29]
	global_load_dwordx4 v[202:205], v19, s[10:11] offset:2048
	global_load_dwordx4 v[206:209], v[28:29], off offset:3072
	global_load_dwordx4 v[210:213], v147, s[28:29]
	global_load_dwordx4 v[228:231], v19, s[10:11] offset:3072
	v_mov_b32_e32 v76, v10
	v_mov_b32_e32 v77, v12
	v_mov_b32_e32 v78, v11
	v_mov_b32_e32 v79, v13
	v_pk_mul_f32 v[76:77], v[76:77], v[56:57] op_sel_hi:[1,0]
	v_pk_mul_f32 v[78:79], v[78:79], v[56:57] op_sel_hi:[1,0]
	v_lshl_add_u64 v[62:63], v[34:35], 0, s[30:31]
	s_waitcnt vmcnt(2)
	v_mov_b32_e32 v80, v64
	v_mov_b32_e32 v81, v66
	v_mov_b32_e32 v66, v65
	v_pk_mul_f32 v[64:65], v[76:77], v[80:81]
	s_waitcnt vmcnt(1)
	v_mov_b32_e32 v76, v68
	v_mov_b32_e32 v77, v70
	v_mov_b32_e32 v70, v69
	s_waitcnt vmcnt(0)
	v_mov_b32_e32 v68, v72
	v_mov_b32_e32 v69, v74
	v_mov_b32_e32 v74, v73
	v_pk_mul_f32 v[66:67], v[78:79], v[66:67]
	v_pk_add_f32 v[68:69], v[68:69], 1.0 op_sel_hi:[1,0]
	v_pk_add_f32 v[72:73], v[74:75], 1.0 op_sel_hi:[1,0]
	v_pk_fma_f32 v[64:65], v[64:65], v[68:69], v[76:77]
	v_pk_fma_f32 v[66:67], v[66:67], v[72:73], v[70:71]
	v_mov_b32_e32 v71, v1
	v_cvt_pk_fp8_f32 v71, v64, v66
	v_and_b32_sdwa v69, v67, v236 dst_sel:DWORD dst_unused:UNUSED_PAD src0_sel:WORD_1 src1_sel:DWORD
	v_and_b32_sdwa v70, v66, v236 dst_sel:DWORD dst_unused:UNUSED_PAD src0_sel:WORD_1 src1_sel:DWORD
	v_and_b32_sdwa v57, v65, v236 dst_sel:DWORD dst_unused:UNUSED_PAD src0_sel:WORD_1 src1_sel:DWORD
	v_cvt_pk_fp8_f32 v71, v65, v67 op_sel:[0,0,1]
	v_and_b32_sdwa v68, v64, v236 dst_sel:DWORD dst_unused:UNUSED_PAD src0_sel:WORD_1 src1_sel:DWORD
	v_add3_u32 v69, v67, v69, s80
	v_add3_u32 v70, v66, v70, s80
	v_add3_u32 v68, v64, v68, s80
	v_add3_u32 v57, v65, v57, s80
	v_and_b32_e32 v64, 0xffff0000, v69
	v_and_b32_e32 v66, 0xffff0000, v70
	v_or_b32_sdwa v69, v64, v57 dst_sel:DWORD dst_unused:UNUSED_PAD src0_sel:DWORD src1_sel:WORD_1
	v_or_b32_sdwa v68, v66, v68 dst_sel:DWORD dst_unused:UNUSED_PAD src0_sel:DWORD src1_sel:WORD_1
	v_lshl_add_u64 v[64:65], v[36:37], 0, s[12:13]
	global_store_dwordx2 v[62:63], v[68:69], off
	global_store_dword v[64:65], v71, off
	s_nop 0
	v_mov_b32_e32 v78, v14
	v_mov_b32_e32 v79, v16
	v_mov_b32_e32 v80, v15
	v_mov_b32_e32 v81, v17
	v_mov_b32_e32 v57, v1
	v_pk_mul_f32 v[78:79], v[78:79], v[56:57] op_sel_hi:[1,0]
	v_pk_mul_f32 v[80:81], v[80:81], v[56:57] op_sel_hi:[1,0]
	s_waitcnt vmcnt(2)
	v_mov_b64_e32 v[66:67], v[182:183]
	v_mov_b64_e32 v[68:69], v[184:185]
	v_mov_b32_e32 v82, v66
	v_mov_b32_e32 v83, v68
	s_waitcnt vmcnt(1)
	v_mov_b64_e32 v[70:71], v[186:187]
	v_mov_b64_e32 v[72:73], v[188:189]
	v_mov_b32_e32 v84, v70
	v_mov_b32_e32 v85, v72
	v_mov_b32_e32 v68, v67
	v_mov_b32_e32 v72, v71
	s_waitcnt vmcnt(0)
	v_mov_b64_e32 v[74:75], v[190:191]
	v_mov_b64_e32 v[76:77], v[192:193]
	v_mov_b32_e32 v86, v74
	v_mov_b32_e32 v87, v76
	v_mov_b32_e32 v76, v75
	v_pk_mul_f32 v[66:67], v[78:79], v[82:83]
	v_pk_add_f32 v[70:71], v[84:85], 1.0 op_sel_hi:[1,0]
	v_pk_mul_f32 v[68:69], v[80:81], v[68:69]
	v_pk_add_f32 v[72:73], v[72:73], 1.0 op_sel_hi:[1,0]
	v_pk_fma_f32 v[66:67], v[66:67], v[70:71], v[86:87]
	v_pk_fma_f32 v[68:69], v[68:69], v[72:73], v[76:77]
	v_and_b32_sdwa v71, v66, v236 dst_sel:DWORD dst_unused:UNUSED_PAD src0_sel:WORD_1 src1_sel:DWORD
	v_cvt_pk_fp8_f32 v57, v66, v68
	v_and_b32_sdwa v72, v69, v236 dst_sel:DWORD dst_unused:UNUSED_PAD src0_sel:WORD_1 src1_sel:DWORD
	v_and_b32_sdwa v73, v68, v236 dst_sel:DWORD dst_unused:UNUSED_PAD src0_sel:WORD_1 src1_sel:DWORD
	v_and_b32_sdwa v70, v67, v236 dst_sel:DWORD dst_unused:UNUSED_PAD src0_sel:WORD_1 src1_sel:DWORD
	v_add3_u32 v66, v66, v71, s80
	v_add3_u32 v71, v69, v72, s80
	v_add3_u32 v68, v68, v73, s80
	v_cvt_pk_fp8_f32 v57, v67, v69 op_sel:[0,0,1]
	v_add3_u32 v70, v67, v70, s80
	v_and_b32_e32 v71, 0xffff0000, v71
	v_and_b32_e32 v68, 0xffff0000, v68
	v_or_b32_sdwa v67, v71, v70 dst_sel:DWORD dst_unused:UNUSED_PAD src0_sel:DWORD src1_sel:WORD_1
	v_or_b32_sdwa v66, v68, v66 dst_sel:DWORD dst_unused:UNUSED_PAD src0_sel:DWORD src1_sel:WORD_1
	global_store_dwordx2 v[62:63], v[66:67], off offset:512
	global_store_dword v[64:65], v57, off offset:256
	s_nop 0
	v_mov_b32_e32 v78, v58
	v_mov_b32_e32 v79, v60
	v_mov_b32_e32 v80, v59
	v_mov_b32_e32 v81, v61
	v_mov_b32_e32 v57, v1
	v_pk_mul_f32 v[78:79], v[78:79], v[56:57] op_sel_hi:[1,0]
	v_pk_mul_f32 v[80:81], v[80:81], v[56:57] op_sel_hi:[1,0]
	s_waitcnt vmcnt(2)
	v_mov_b64_e32 v[66:67], v[194:195]
	v_mov_b64_e32 v[68:69], v[196:197]
	v_mov_b32_e32 v82, v66
	v_mov_b32_e32 v83, v68
	s_waitcnt vmcnt(1)
	v_mov_b64_e32 v[70:71], v[198:199]
	v_mov_b64_e32 v[72:73], v[200:201]
	v_mov_b32_e32 v84, v70
	v_mov_b32_e32 v85, v72
	v_mov_b32_e32 v68, v67
	v_mov_b32_e32 v72, v71
	s_waitcnt vmcnt(0)
	v_mov_b64_e32 v[74:75], v[202:203]
	v_mov_b64_e32 v[76:77], v[204:205]
	v_mov_b32_e32 v86, v74
	v_mov_b32_e32 v87, v76
	v_mov_b32_e32 v76, v75
	v_pk_mul_f32 v[66:67], v[78:79], v[82:83]
	v_pk_add_f32 v[70:71], v[84:85], 1.0 op_sel_hi:[1,0]
	v_pk_mul_f32 v[68:69], v[80:81], v[68:69]
	v_pk_add_f32 v[72:73], v[72:73], 1.0 op_sel_hi:[1,0]
	v_pk_fma_f32 v[66:67], v[66:67], v[70:71], v[86:87]
	v_pk_fma_f32 v[68:69], v[68:69], v[72:73], v[76:77]
	v_and_b32_sdwa v71, v66, v236 dst_sel:DWORD dst_unused:UNUSED_PAD src0_sel:WORD_1 src1_sel:DWORD
	v_cvt_pk_fp8_f32 v57, v66, v68
	v_and_b32_sdwa v72, v69, v236 dst_sel:DWORD dst_unused:UNUSED_PAD src0_sel:WORD_1 src1_sel:DWORD
	v_and_b32_sdwa v73, v68, v236 dst_sel:DWORD dst_unused:UNUSED_PAD src0_sel:WORD_1 src1_sel:DWORD
	v_and_b32_sdwa v70, v67, v236 dst_sel:DWORD dst_unused:UNUSED_PAD src0_sel:WORD_1 src1_sel:DWORD
	v_add3_u32 v66, v66, v71, s80
	v_add3_u32 v71, v69, v72, s80
	v_add3_u32 v68, v68, v73, s80
	v_cvt_pk_fp8_f32 v57, v67, v69 op_sel:[0,0,1]
	v_add3_u32 v70, v67, v70, s80
	v_and_b32_e32 v71, 0xffff0000, v71
	v_and_b32_e32 v68, 0xffff0000, v68
	v_or_b32_sdwa v67, v71, v70 dst_sel:DWORD dst_unused:UNUSED_PAD src0_sel:DWORD src1_sel:WORD_1
	v_or_b32_sdwa v66, v68, v66 dst_sel:DWORD dst_unused:UNUSED_PAD src0_sel:DWORD src1_sel:WORD_1
	global_store_dwordx2 v[62:63], v[66:67], off offset:1024
	global_store_dword v[64:65], v57, off offset:512
	s_nop 0
	v_mov_b32_e32 v78, v6
	v_mov_b32_e32 v79, v8
	v_mov_b32_e32 v80, v7
	v_mov_b32_e32 v81, v9
	v_mov_b32_e32 v57, v1
	v_pk_mul_f32 v[78:79], v[78:79], v[56:57] op_sel_hi:[1,0]
	v_pk_mul_f32 v[80:81], v[80:81], v[56:57] op_sel_hi:[1,0]
	s_mov_b64 s[10:11], 0
	s_waitcnt vmcnt(2)
	v_mov_b64_e32 v[66:67], v[206:207]
	v_mov_b64_e32 v[68:69], v[208:209]
	v_mov_b32_e32 v82, v66
	v_mov_b32_e32 v83, v68
	s_waitcnt vmcnt(1)
	v_mov_b64_e32 v[70:71], v[210:211]
	v_mov_b64_e32 v[72:73], v[212:213]
	v_mov_b32_e32 v84, v70
	v_mov_b32_e32 v85, v72
	v_mov_b32_e32 v68, v67
	v_mov_b32_e32 v72, v71
	s_waitcnt vmcnt(0)
	v_mov_b64_e32 v[74:75], v[228:229]
	v_mov_b64_e32 v[76:77], v[230:231]
	v_mov_b32_e32 v86, v74
	v_mov_b32_e32 v87, v76
	v_mov_b32_e32 v76, v75
	v_pk_mul_f32 v[66:67], v[78:79], v[82:83]
	v_pk_add_f32 v[70:71], v[84:85], 1.0 op_sel_hi:[1,0]
	v_pk_mul_f32 v[68:69], v[80:81], v[68:69]
	v_pk_add_f32 v[72:73], v[72:73], 1.0 op_sel_hi:[1,0]
	v_pk_fma_f32 v[66:67], v[66:67], v[70:71], v[86:87]
	v_pk_fma_f32 v[68:69], v[68:69], v[72:73], v[76:77]
	v_and_b32_sdwa v71, v66, v236 dst_sel:DWORD dst_unused:UNUSED_PAD src0_sel:WORD_1 src1_sel:DWORD
	v_cvt_pk_fp8_f32 v57, v66, v68
	v_and_b32_sdwa v72, v69, v236 dst_sel:DWORD dst_unused:UNUSED_PAD src0_sel:WORD_1 src1_sel:DWORD
	v_and_b32_sdwa v73, v68, v236 dst_sel:DWORD dst_unused:UNUSED_PAD src0_sel:WORD_1 src1_sel:DWORD
	v_and_b32_sdwa v70, v67, v236 dst_sel:DWORD dst_unused:UNUSED_PAD src0_sel:WORD_1 src1_sel:DWORD
	v_add3_u32 v66, v66, v71, s80
	v_add3_u32 v71, v69, v72, s80
	v_add3_u32 v68, v68, v73, s80
	v_cvt_pk_fp8_f32 v57, v67, v69 op_sel:[0,0,1]
	v_add3_u32 v70, v67, v70, s80
	v_and_b32_e32 v71, 0xffff0000, v71
	v_and_b32_e32 v68, 0xffff0000, v68
	v_or_b32_sdwa v67, v71, v70 dst_sel:DWORD dst_unused:UNUSED_PAD src0_sel:DWORD src1_sel:WORD_1
	v_or_b32_sdwa v66, v68, v66 dst_sel:DWORD dst_unused:UNUSED_PAD src0_sel:DWORD src1_sel:WORD_1
	global_store_dwordx2 v[62:63], v[66:67], off offset:1536
	global_store_dword v[64:65], v57, off offset:768
.LBB0_2163:
	s_andn2_b64 vcc, exec, s[10:11]
	s_cbranch_vccnz .LBB0_2165
	global_load_dwordx4 v[62:65], v[30:31], off
	global_load_dwordx4 v[170:173], v[30:31], off offset:1024
	global_load_dwordx4 v[174:177], v[30:31], off offset:2048
	global_load_dwordx4 v[178:181], v[30:31], off offset:3072
	v_pk_mul_f32 v[10:11], v[10:11], v[56:57] op_sel_hi:[1,0]
	v_pk_mul_f32 v[12:13], v[12:13], v[56:57] op_sel_hi:[1,0]
	v_lshl_add_u64 v[66:67], s[12:13], 2, v[38:39]
	v_pk_mul_f32 v[14:15], v[14:15], v[56:57] op_sel_hi:[1,0]
	v_pk_mul_f32 v[16:17], v[16:17], v[56:57] op_sel_hi:[1,0]
	v_pk_mul_f32 v[6:7], v[6:7], v[56:57] op_sel_hi:[1,0]
	v_pk_mul_f32 v[8:9], v[8:9], v[56:57] op_sel_hi:[1,0]
	s_waitcnt vmcnt(0)
	v_pk_mul_f32 v[10:11], v[10:11], v[62:63]
	v_pk_mul_f32 v[12:13], v[12:13], v[64:65]
	global_store_dwordx4 v[66:67], v[10:13], off
	s_waitcnt vmcnt(0)
	v_mov_b64_e32 v[10:11], v[170:171]
	v_mov_b64_e32 v[12:13], v[172:173]
	v_pk_mul_f32 v[10:11], v[14:15], v[10:11]
	v_pk_mul_f32 v[12:13], v[16:17], v[12:13]
	global_store_dwordx4 v[66:67], v[10:13], off offset:1024
	v_pk_mul_f32 v[14:15], v[58:59], v[56:57] op_sel_hi:[1,0]
	v_pk_mul_f32 v[16:17], v[60:61], v[56:57] op_sel_hi:[1,0]
	s_waitcnt vmcnt(0)
	v_mov_b64_e32 v[10:11], v[174:175]
	v_mov_b64_e32 v[12:13], v[176:177]
	v_pk_mul_f32 v[10:11], v[14:15], v[10:11]
	v_pk_mul_f32 v[12:13], v[16:17], v[12:13]
	global_store_dwordx4 v[66:67], v[10:13], off offset:2048
	s_waitcnt vmcnt(0)
	v_mov_b64_e32 v[10:11], v[178:179]
	v_mov_b64_e32 v[12:13], v[180:181]
	v_pk_mul_f32 v[6:7], v[6:7], v[10:11]
	v_pk_mul_f32 v[8:9], v[8:9], v[12:13]
	global_store_dwordx4 v[66:67], v[6:9], off offset:3072
.LBB0_2165:
	v_readlane_b32 s9, v254, 46
	s_cmp_ge_i32 s8, s9
	s_cbranch_scc1 .LBB0_2150
	s_ashr_i32 s9, s8, 31
	s_lshl_b64 s[10:11], s[8:9], 10
	s_lshr_b32 s9, s9, 20
	s_add_i32 s9, s8, s9
	s_ashr_i32 s9, s9, 12
	s_cmp_lt_i32 s8, 0x8000
	s_cselect_b32 s12, s9, 8
	s_ashr_i32 s13, s12, 31
	s_add_u32 s8, s12, s41
	v_mul_f32_e32 v62, 0x3e000000, v2
	v_mul_f32_e32 v60, 0x3e000000, v3
	s_addc_u32 s9, s13, 0
	v_cvt_pk_f32_fp8_e32 v[2:3], v135
	v_mul_f32_e32 v58, 0x3e000000, v4
	v_mul_f32_e32 v56, 0x3e000000, v5
	s_mulk_i32 s9, 0x6000
	s_mul_hi_u32 s23, s8, 0x6000
	v_cvt_pk_f32_fp8_e32 v[4:5], v136
	s_add_i32 s23, s23, s9
	s_mulk_i32 s8, 0x6000
	v_readlane_b32 s26, v252, 4
	v_cvt_pk_f32_fp8_e32 v[6:7], v137
	v_readlane_b32 s27, v252, 5
	s_add_u32 s8, s26, s8
	v_cvt_pk_f32_fp8_e32 v[14:15], v138
	s_addc_u32 s9, s27, s23
	v_pk_fma_f32 v[2:3], v[62:63], v[2:3], 0 op_sel_hi:[0,1,0]
	s_add_u32 s8, s8, 0x105000
	v_pk_fma_f32 v[2:3], v[60:61], v[4:5], v[2:3] op_sel_hi:[0,1,1]
	s_addc_u32 s9, s9, 0
	v_pk_fma_f32 v[2:3], v[58:59], v[6:7], v[2:3] op_sel_hi:[0,1,1]
	v_pk_fma_f32 v[6:7], v[56:57], v[14:15], v[2:3] op_sel_hi:[0,1,1]
	global_load_dwordx4 v[2:5], v19, s[8:9]
	global_load_dwordx4 v[170:173], v129, s[8:9]
	global_load_dwordx4 v[174:177], v134, s[8:9]
	global_load_dwordx4 v[178:181], v147, s[8:9]
	v_cvt_pk_f32_fp8_sdwa v[8:9], v135 src0_sel:WORD_1
	v_cvt_pk_f32_fp8_sdwa v[10:11], v136 src0_sel:WORD_1
	v_cvt_pk_f32_fp8_sdwa v[12:13], v137 src0_sel:WORD_1
	v_cvt_pk_f32_fp8_sdwa v[16:17], v138 src0_sel:WORD_1
	v_lshlrev_b32_e32 v64, 16, v48
	v_and_b32_e32 v65, 0xffff0000, v48
	v_lshlrev_b32_e32 v48, 16, v49
	v_and_b32_e32 v49, 0xffff0000, v49
	v_cvt_pk_f32_fp8_e32 v[66:67], v133
	v_cvt_pk_f32_fp8_sdwa v[14:15], v131 src0_sel:WORD_1
	v_cvt_pk_f32_fp8_sdwa v[68:69], v133 src0_sel:WORD_1
	v_lshlrev_b32_e32 v70, 16, v54
	v_and_b32_e32 v71, 0xffff0000, v54
	v_lshlrev_b32_e32 v54, 16, v55
	v_and_b32_e32 v55, 0xffff0000, v55
	v_cvt_pk_f32_fp8_e32 v[72:73], v125
	v_cvt_pk_f32_fp8_sdwa v[74:75], v125 src0_sel:WORD_1
	v_lshlrev_b32_e32 v76, 16, v52
	v_and_b32_e32 v77, 0xffff0000, v52
	v_lshlrev_b32_e32 v52, 16, v53
	v_and_b32_e32 v53, 0xffff0000, v53
	v_cvt_pk_f32_fp8_e32 v[80:81], v25
	v_cvt_pk_f32_fp8_e32 v[82:83], v21
	v_lshlrev_b32_e32 v78, 16, v50
	v_and_b32_e32 v79, 0xffff0000, v50
	v_lshlrev_b32_e32 v50, 16, v51
	v_and_b32_e32 v51, 0xffff0000, v51
	v_readlane_b32 s26, v254, 44
	v_readlane_b32 s27, v254, 45
	s_waitcnt vmcnt(0)
	v_pk_fma_f32 v[6:7], v[2:3], v[6:7], v[64:65]
	v_pk_fma_f32 v[2:3], v[62:63], v[8:9], 0 op_sel_hi:[0,1,0]
	v_pk_fma_f32 v[2:3], v[60:61], v[10:11], v[2:3] op_sel_hi:[0,1,1]
	v_pk_fma_f32 v[2:3], v[58:59], v[12:13], v[2:3] op_sel_hi:[0,1,1]
	v_pk_fma_f32 v[2:3], v[56:57], v[16:17], v[2:3] op_sel_hi:[0,1,1]
	v_pk_fma_f32 v[8:9], v[2:3], v[4:5], v[48:49]
	v_cvt_pk_f32_fp8_e32 v[2:3], v130
	v_cvt_pk_f32_fp8_e32 v[4:5], v131
	v_cvt_pk_f32_fp8_e32 v[10:11], v132
	v_cvt_pk_f32_fp8_sdwa v[12:13], v130 src0_sel:WORD_1
	v_pk_fma_f32 v[2:3], v[62:63], v[2:3], 0 op_sel_hi:[0,1,0]
	v_pk_fma_f32 v[2:3], v[60:61], v[4:5], v[2:3] op_sel_hi:[0,1,1]
	v_pk_fma_f32 v[2:3], v[58:59], v[10:11], v[2:3] op_sel_hi:[0,1,1]
	v_pk_fma_f32 v[10:11], v[56:57], v[66:67], v[2:3] op_sel_hi:[0,1,1]
	v_cvt_pk_f32_fp8_sdwa v[16:17], v132 src0_sel:WORD_1
	v_pk_mul_f32 v[64:65], v[6:7], v[6:7]
	v_pk_mul_f32 v[48:49], v[8:9], v[8:9]
	s_waitcnt vmcnt(0)
	v_mov_b64_e32 v[2:3], v[170:171]
	v_mov_b64_e32 v[4:5], v[172:173]
	v_pk_fma_f32 v[10:11], v[2:3], v[10:11], v[70:71]
	v_pk_fma_f32 v[2:3], v[62:63], v[12:13], 0 op_sel_hi:[0,1,0]
	v_pk_fma_f32 v[2:3], v[60:61], v[14:15], v[2:3] op_sel_hi:[0,1,1]
	v_pk_fma_f32 v[2:3], v[58:59], v[16:17], v[2:3] op_sel_hi:[0,1,1]
	v_pk_fma_f32 v[2:3], v[56:57], v[68:69], v[2:3] op_sel_hi:[0,1,1]
	v_pk_fma_f32 v[12:13], v[2:3], v[4:5], v[54:55]
	v_cvt_pk_f32_fp8_e32 v[2:3], v128
	v_cvt_pk_f32_fp8_e32 v[4:5], v127
	v_cvt_pk_f32_fp8_e32 v[14:15], v126
	v_cvt_pk_f32_fp8_sdwa v[16:17], v128 src0_sel:WORD_1
	v_pk_fma_f32 v[2:3], v[62:63], v[2:3], 0 op_sel_hi:[0,1,0]
	v_pk_fma_f32 v[2:3], v[60:61], v[4:5], v[2:3] op_sel_hi:[0,1,1]
	v_pk_fma_f32 v[2:3], v[58:59], v[14:15], v[2:3] op_sel_hi:[0,1,1]
	v_pk_fma_f32 v[14:15], v[56:57], v[72:73], v[2:3] op_sel_hi:[0,1,1]
	v_cvt_pk_f32_fp8_sdwa v[68:69], v127 src0_sel:WORD_1
	v_cvt_pk_f32_fp8_sdwa v[70:71], v126 src0_sel:WORD_1
	v_cvt_pk_f32_fp8_sdwa v[72:73], v27 src0_sel:WORD_1
	v_pk_mul_f32 v[66:67], v[10:11], v[10:11]
	v_pk_mul_f32 v[54:55], v[12:13], v[12:13]
	s_waitcnt vmcnt(0)
	v_mov_b64_e32 v[2:3], v[174:175]
	v_mov_b64_e32 v[4:5], v[176:177]
	v_pk_fma_f32 v[14:15], v[2:3], v[14:15], v[76:77]
	v_pk_fma_f32 v[2:3], v[62:63], v[16:17], 0 op_sel_hi:[0,1,0]
	v_pk_fma_f32 v[2:3], v[60:61], v[68:69], v[2:3] op_sel_hi:[0,1,1]
	v_pk_fma_f32 v[2:3], v[58:59], v[70:71], v[2:3] op_sel_hi:[0,1,1]
	v_pk_fma_f32 v[2:3], v[56:57], v[74:75], v[2:3] op_sel_hi:[0,1,1]
	v_pk_fma_f32 v[16:17], v[2:3], v[4:5], v[52:53]
	v_cvt_pk_f32_fp8_e32 v[2:3], v124
	v_cvt_pk_f32_fp8_e32 v[4:5], v27
	v_cvt_pk_f32_fp8_sdwa v[70:71], v124 src0_sel:WORD_1
	v_cvt_pk_f32_fp8_sdwa v[74:75], v25 src0_sel:WORD_1
	v_pk_fma_f32 v[2:3], v[62:63], v[2:3], 0 op_sel_hi:[0,1,0]
	v_pk_fma_f32 v[2:3], v[60:61], v[4:5], v[2:3] op_sel_hi:[0,1,1]
	v_pk_fma_f32 v[2:3], v[58:59], v[80:81], v[2:3] op_sel_hi:[0,1,1]
	v_pk_fma_f32 v[80:81], v[56:57], v[82:83], v[2:3] op_sel_hi:[0,1,1]
	v_cvt_pk_f32_fp8_sdwa v[76:77], v21 src0_sel:WORD_1
	v_add_f32_e32 v21, v66, v67
	v_add_f32_e32 v25, v64, v65
	v_pk_fma_f32 v[62:63], v[62:63], v[70:71], 0 op_sel_hi:[0,1,0]
	v_add_f32_e32 v21, v21, v54
	v_add_f32_e32 v25, v25, v48
	v_pk_mul_f32 v[68:69], v[14:15], v[14:15]
	v_pk_fma_f32 v[60:61], v[60:61], v[72:73], v[62:63] op_sel_hi:[0,1,1]
	v_add_f32_e32 v21, v55, v21
	v_add_f32_e32 v25, v49, v25
	v_pk_mul_f32 v[52:53], v[16:17], v[16:17]
	v_pk_fma_f32 v[58:59], v[58:59], v[74:75], v[60:61] op_sel_hi:[0,1,1]
	v_add_f32_e32 v21, v25, v21
	v_add_f32_e32 v25, v68, v69
	v_pk_fma_f32 v[56:57], v[56:57], v[76:77], v[58:59] op_sel_hi:[0,1,1]
	v_add_f32_e32 v25, v25, v52
	v_add_f32_e32 v25, v53, v25
	v_add_f32_e32 v21, v21, v25
	s_mov_b32 s8, 0x800000
	s_waitcnt vmcnt(0)
	v_mov_b64_e32 v[2:3], v[178:179]
	v_mov_b64_e32 v[4:5], v[180:181]
	v_pk_fma_f32 v[2:3], v[2:3], v[80:81], v[78:79]
	v_pk_fma_f32 v[4:5], v[56:57], v[4:5], v[50:51]
	v_pk_mul_f32 v[50:51], v[2:3], v[2:3]
	v_pk_mul_f32 v[56:57], v[4:5], v[4:5]
	v_add_f32_e32 v25, v50, v51
	v_add_f32_e32 v25, v25, v56
	v_add_f32_e32 v25, v57, v25
	v_add_f32_e32 v21, v21, v25
	s_nop 1
	v_add_f32_dpp v21, v21, v21 row_ror:1 row_mask:0xf bank_mask:0xf bound_ctrl:1
	s_nop 1
	v_add_f32_dpp v21, v21, v21 row_ror:2 row_mask:0xf bank_mask:0xf bound_ctrl:1
	s_nop 1
	v_add_f32_dpp v21, v21, v21 row_ror:4 row_mask:0xf bank_mask:0xf bound_ctrl:1
	s_nop 1
	v_add_f32_dpp v21, v21, v21 row_ror:8 row_mask:0xf bank_mask:0xf bound_ctrl:1
	v_mov_b32_e32 v25, v21
	s_nop 1
	v_permlane16_swap_b32_e32 v21, v25
	v_add_f32_e32 v21, v21, v25
	v_mov_b32_e32 v25, v21
	s_nop 1
	v_permlane32_swap_b32_e32 v21, v25
	v_add_f32_e32 v21, v21, v25
	v_fmamk_f32 v21, v21, 0x3a800000, v237
	v_cmp_gt_f32_e32 vcc, s8, v21
	v_mul_f32_e32 v25, 0x4b800000, v21
	s_mov_b64 s[8:9], -1
	v_cndmask_b32_e32 v21, v21, v25, vcc
	v_rsq_f32_e32 v21, v21
	s_nop 0
	v_mul_f32_e32 v25, 0x45800000, v21
	v_cndmask_b32_e32 v48, v21, v25, vcc
	s_and_b64 vcc, exec, s[26:27]
	s_cbranch_vccz .LBB0_2168
	v_and_b32_sdwa v27, v9, v236 dst_sel:DWORD dst_unused:UNUSED_PAD src0_sel:WORD_1 src1_sel:DWORD
	v_and_b32_sdwa v49, v7, v236 dst_sel:DWORD dst_unused:UNUSED_PAD src0_sel:WORD_1 src1_sel:DWORD
	v_and_b32_sdwa v21, v8, v236 dst_sel:DWORD dst_unused:UNUSED_PAD src0_sel:WORD_1 src1_sel:DWORD
	v_and_b32_sdwa v25, v6, v236 dst_sel:DWORD dst_unused:UNUSED_PAD src0_sel:WORD_1 src1_sel:DWORD
	v_add3_u32 v27, v9, v27, s80
	v_add3_u32 v49, v7, v49, s80
	v_add3_u32 v25, v6, v25, s80
	v_add3_u32 v21, v8, v21, s80
	v_and_b32_e32 v27, 0xffff0000, v27
	v_and_b32_e32 v49, 0xffff0000, v49
	v_or_b32_sdwa v53, v27, v21 dst_sel:DWORD dst_unused:UNUSED_PAD src0_sel:DWORD src1_sel:WORD_1
	v_or_b32_sdwa v52, v49, v25 dst_sel:DWORD dst_unused:UNUSED_PAD src0_sel:DWORD src1_sel:WORD_1
	v_and_b32_sdwa v27, v13, v236 dst_sel:DWORD dst_unused:UNUSED_PAD src0_sel:WORD_1 src1_sel:DWORD
	v_and_b32_sdwa v49, v11, v236 dst_sel:DWORD dst_unused:UNUSED_PAD src0_sel:WORD_1 src1_sel:DWORD
	s_lshl_b64 s[28:29], s[10:11], 1
	v_and_b32_sdwa v21, v12, v236 dst_sel:DWORD dst_unused:UNUSED_PAD src0_sel:WORD_1 src1_sel:DWORD
	v_and_b32_sdwa v25, v10, v236 dst_sel:DWORD dst_unused:UNUSED_PAD src0_sel:WORD_1 src1_sel:DWORD
	v_add3_u32 v27, v13, v27, s80
	v_add3_u32 v49, v11, v49, s80
	v_lshl_add_u64 v[50:51], v[32:33], 0, s[28:29]
	v_add3_u32 v25, v10, v25, s80
	v_add3_u32 v21, v12, v21, s80
	v_and_b32_e32 v27, 0xffff0000, v27
	v_and_b32_e32 v49, 0xffff0000, v49
	global_store_dwordx2 v[50:51], v[52:53], off
	v_or_b32_sdwa v53, v27, v21 dst_sel:DWORD dst_unused:UNUSED_PAD src0_sel:DWORD src1_sel:WORD_1
	v_or_b32_sdwa v52, v49, v25 dst_sel:DWORD dst_unused:UNUSED_PAD src0_sel:DWORD src1_sel:WORD_1
	v_and_b32_sdwa v27, v17, v236 dst_sel:DWORD dst_unused:UNUSED_PAD src0_sel:WORD_1 src1_sel:DWORD
	v_and_b32_sdwa v49, v15, v236 dst_sel:DWORD dst_unused:UNUSED_PAD src0_sel:WORD_1 src1_sel:DWORD
	v_and_b32_sdwa v21, v16, v236 dst_sel:DWORD dst_unused:UNUSED_PAD src0_sel:WORD_1 src1_sel:DWORD
	v_and_b32_sdwa v25, v14, v236 dst_sel:DWORD dst_unused:UNUSED_PAD src0_sel:WORD_1 src1_sel:DWORD
	v_add3_u32 v27, v17, v27, s80
	v_add3_u32 v49, v15, v49, s80
	s_add_u32 s8, s12, s42
	v_add3_u32 v25, v14, v25, s80
	v_add3_u32 v21, v16, v21, s80
	v_and_b32_e32 v27, 0xffff0000, v27
	v_and_b32_e32 v49, 0xffff0000, v49
	s_addc_u32 s9, s13, 0
	global_store_dwordx2 v[50:51], v[52:53], off offset:512
	v_or_b32_sdwa v53, v27, v21 dst_sel:DWORD dst_unused:UNUSED_PAD src0_sel:DWORD src1_sel:WORD_1
	v_or_b32_sdwa v52, v49, v25 dst_sel:DWORD dst_unused:UNUSED_PAD src0_sel:DWORD src1_sel:WORD_1
	v_and_b32_sdwa v27, v5, v236 dst_sel:DWORD dst_unused:UNUSED_PAD src0_sel:WORD_1 src1_sel:DWORD
	v_and_b32_sdwa v49, v3, v236 dst_sel:DWORD dst_unused:UNUSED_PAD src0_sel:WORD_1 src1_sel:DWORD
	s_mulk_i32 s9, 0x6000
	s_mul_hi_u32 s12, s8, 0x6000
	v_and_b32_sdwa v21, v4, v236 dst_sel:DWORD dst_unused:UNUSED_PAD src0_sel:WORD_1 src1_sel:DWORD
	v_and_b32_sdwa v25, v2, v236 dst_sel:DWORD dst_unused:UNUSED_PAD src0_sel:WORD_1 src1_sel:DWORD
	v_add3_u32 v27, v5, v27, s80
	v_add3_u32 v49, v3, v49, s80
	s_add_i32 s12, s12, s9
	s_mulk_i32 s8, 0x6000
	v_readlane_b32 s9, v253, 8
	v_add3_u32 v25, v2, v25, s80
	v_add3_u32 v21, v4, v21, s80
	v_and_b32_e32 v27, 0xffff0000, v27
	v_and_b32_e32 v49, 0xffff0000, v49
	s_add_u32 s8, s9, s8
	v_readlane_b32 s9, v253, 9
	global_store_dwordx2 v[50:51], v[52:53], off offset:1024
	v_or_b32_sdwa v53, v27, v21 dst_sel:DWORD dst_unused:UNUSED_PAD src0_sel:DWORD src1_sel:WORD_1
	v_or_b32_sdwa v52, v49, v25 dst_sel:DWORD dst_unused:UNUSED_PAD src0_sel:DWORD src1_sel:WORD_1
	s_addc_u32 s9, s9, s12
	global_store_dwordx2 v[50:51], v[52:53], off offset:1536
	s_add_u32 s12, s8, 0x1000
	global_load_dwordx4 v[52:55], v[28:29], off
	s_addc_u32 s13, s9, 0
	global_load_dwordx4 v[56:59], v19, s[8:9]
	global_load_dwordx4 v[60:63], v19, s[12:13]
	global_load_dwordx4 v[182:185], v[28:29], off offset:1024
	global_load_dwordx4 v[186:189], v129, s[12:13]
	global_load_dwordx4 v[190:193], v19, s[8:9] offset:1024
	global_load_dwordx4 v[194:197], v[28:29], off offset:2048
	global_load_dwordx4 v[198:201], v134, s[12:13]
	global_load_dwordx4 v[202:205], v19, s[8:9] offset:2048
	global_load_dwordx4 v[206:209], v[28:29], off offset:3072
	global_load_dwordx4 v[210:213], v147, s[12:13]
	global_load_dwordx4 v[228:231], v19, s[8:9] offset:3072
	v_mov_b32_e32 v64, v6
	v_mov_b32_e32 v65, v8
	v_mov_b32_e32 v66, v7
	v_mov_b32_e32 v67, v9
	v_pk_mul_f32 v[64:65], v[64:65], v[48:49] op_sel_hi:[1,0]
	v_pk_mul_f32 v[66:67], v[66:67], v[48:49] op_sel_hi:[1,0]
	v_lshl_add_u64 v[50:51], v[34:35], 0, s[28:29]
	s_waitcnt vmcnt(2)
	v_mov_b32_e32 v68, v52
	v_mov_b32_e32 v69, v54
	v_mov_b32_e32 v54, v53
	v_pk_mul_f32 v[52:53], v[64:65], v[68:69]
	s_waitcnt vmcnt(1)
	v_mov_b32_e32 v64, v56
	v_mov_b32_e32 v65, v58
	v_mov_b32_e32 v58, v57
	s_waitcnt vmcnt(0)
	v_mov_b32_e32 v56, v60
	v_mov_b32_e32 v57, v62
	v_mov_b32_e32 v62, v61
	v_pk_mul_f32 v[54:55], v[66:67], v[54:55]
	v_pk_add_f32 v[56:57], v[56:57], 1.0 op_sel_hi:[1,0]
	v_pk_add_f32 v[60:61], v[62:63], 1.0 op_sel_hi:[1,0]
	v_pk_fma_f32 v[52:53], v[52:53], v[56:57], v[64:65]
	v_pk_fma_f32 v[54:55], v[54:55], v[60:61], v[58:59]
	v_mov_b32_e32 v58, v1
	v_cvt_pk_fp8_f32 v58, v52, v54
	v_and_b32_sdwa v27, v55, v236 dst_sel:DWORD dst_unused:UNUSED_PAD src0_sel:WORD_1 src1_sel:DWORD
	v_and_b32_sdwa v49, v54, v236 dst_sel:DWORD dst_unused:UNUSED_PAD src0_sel:WORD_1 src1_sel:DWORD
	v_and_b32_sdwa v21, v53, v236 dst_sel:DWORD dst_unused:UNUSED_PAD src0_sel:WORD_1 src1_sel:DWORD
	v_cvt_pk_fp8_f32 v58, v53, v55 op_sel:[0,0,1]
	v_and_b32_sdwa v25, v52, v236 dst_sel:DWORD dst_unused:UNUSED_PAD src0_sel:WORD_1 src1_sel:DWORD
	v_add3_u32 v27, v55, v27, s80
	v_add3_u32 v49, v54, v49, s80
	v_add3_u32 v25, v52, v25, s80
	v_add3_u32 v21, v53, v21, s80
	v_and_b32_e32 v27, 0xffff0000, v27
	v_and_b32_e32 v49, 0xffff0000, v49
	v_or_b32_sdwa v57, v27, v21 dst_sel:DWORD dst_unused:UNUSED_PAD src0_sel:DWORD src1_sel:WORD_1
	v_or_b32_sdwa v56, v49, v25 dst_sel:DWORD dst_unused:UNUSED_PAD src0_sel:DWORD src1_sel:WORD_1
	v_lshl_add_u64 v[52:53], v[36:37], 0, s[10:11]
	global_store_dwordx2 v[50:51], v[56:57], off
	global_store_dword v[52:53], v58, off
	s_nop 0
	v_mov_b32_e32 v66, v10
	v_mov_b32_e32 v67, v12
	v_mov_b32_e32 v68, v11
	v_mov_b32_e32 v69, v13
	v_pk_mul_f32 v[66:67], v[66:67], v[48:49] op_sel_hi:[1,0]
	v_pk_mul_f32 v[68:69], v[68:69], v[48:49] op_sel_hi:[1,0]
	v_mov_b32_e32 v21, v1
	s_waitcnt vmcnt(2)
	v_mov_b64_e32 v[54:55], v[182:183]
	v_mov_b64_e32 v[56:57], v[184:185]
	v_mov_b32_e32 v70, v54
	v_mov_b32_e32 v71, v56
	s_waitcnt vmcnt(1)
	v_mov_b64_e32 v[58:59], v[186:187]
	v_mov_b64_e32 v[60:61], v[188:189]
	v_mov_b32_e32 v72, v58
	v_mov_b32_e32 v73, v60
	v_mov_b32_e32 v56, v55
	v_mov_b32_e32 v60, v59
	s_waitcnt vmcnt(0)
	v_mov_b64_e32 v[62:63], v[190:191]
	v_mov_b64_e32 v[64:65], v[192:193]
	v_mov_b32_e32 v74, v62
	v_mov_b32_e32 v75, v64
	v_mov_b32_e32 v64, v63
	v_pk_mul_f32 v[54:55], v[66:67], v[70:71]
	v_pk_add_f32 v[58:59], v[72:73], 1.0 op_sel_hi:[1,0]
	v_pk_mul_f32 v[56:57], v[68:69], v[56:57]
	v_pk_add_f32 v[60:61], v[60:61], 1.0 op_sel_hi:[1,0]
	v_pk_fma_f32 v[54:55], v[54:55], v[58:59], v[74:75]
	v_pk_fma_f32 v[56:57], v[56:57], v[60:61], v[64:65]
	v_and_b32_sdwa v27, v54, v236 dst_sel:DWORD dst_unused:UNUSED_PAD src0_sel:WORD_1 src1_sel:DWORD
	v_cvt_pk_fp8_f32 v21, v54, v56
	v_and_b32_sdwa v49, v57, v236 dst_sel:DWORD dst_unused:UNUSED_PAD src0_sel:WORD_1 src1_sel:DWORD
	v_and_b32_sdwa v58, v56, v236 dst_sel:DWORD dst_unused:UNUSED_PAD src0_sel:WORD_1 src1_sel:DWORD
	v_and_b32_sdwa v25, v55, v236 dst_sel:DWORD dst_unused:UNUSED_PAD src0_sel:WORD_1 src1_sel:DWORD
	v_add3_u32 v27, v54, v27, s80
	v_add3_u32 v49, v57, v49, s80
	v_add3_u32 v54, v56, v58, s80
	v_cvt_pk_fp8_f32 v21, v55, v57 op_sel:[0,0,1]
	v_add3_u32 v25, v55, v25, s80
	v_and_b32_e32 v49, 0xffff0000, v49
	v_and_b32_e32 v54, 0xffff0000, v54
	v_or_b32_sdwa v55, v49, v25 dst_sel:DWORD dst_unused:UNUSED_PAD src0_sel:DWORD src1_sel:WORD_1
	v_or_b32_sdwa v54, v54, v27 dst_sel:DWORD dst_unused:UNUSED_PAD src0_sel:DWORD src1_sel:WORD_1
	global_store_dwordx2 v[50:51], v[54:55], off offset:512
	global_store_dword v[52:53], v21, off offset:256
	s_nop 0
	v_mov_b32_e32 v66, v14
	v_mov_b32_e32 v67, v16
	v_mov_b32_e32 v68, v15
	v_mov_b32_e32 v69, v17
	v_pk_mul_f32 v[66:67], v[66:67], v[48:49] op_sel_hi:[1,0]
	v_pk_mul_f32 v[68:69], v[68:69], v[48:49] op_sel_hi:[1,0]
	v_mov_b32_e32 v21, v1
	s_waitcnt vmcnt(2)
	v_mov_b64_e32 v[54:55], v[194:195]
	v_mov_b64_e32 v[56:57], v[196:197]
	v_mov_b32_e32 v70, v54
	v_mov_b32_e32 v71, v56
	s_waitcnt vmcnt(1)
	v_mov_b64_e32 v[58:59], v[198:199]
	v_mov_b64_e32 v[60:61], v[200:201]
	v_mov_b32_e32 v72, v58
	v_mov_b32_e32 v73, v60
	v_mov_b32_e32 v56, v55
	v_mov_b32_e32 v60, v59
	s_waitcnt vmcnt(0)
	v_mov_b64_e32 v[62:63], v[202:203]
	v_mov_b64_e32 v[64:65], v[204:205]
	v_mov_b32_e32 v74, v62
	v_mov_b32_e32 v75, v64
	v_mov_b32_e32 v64, v63
	v_pk_mul_f32 v[54:55], v[66:67], v[70:71]
	v_pk_add_f32 v[58:59], v[72:73], 1.0 op_sel_hi:[1,0]
	v_pk_mul_f32 v[56:57], v[68:69], v[56:57]
	v_pk_add_f32 v[60:61], v[60:61], 1.0 op_sel_hi:[1,0]
	v_pk_fma_f32 v[54:55], v[54:55], v[58:59], v[74:75]
	v_pk_fma_f32 v[56:57], v[56:57], v[60:61], v[64:65]
	v_and_b32_sdwa v27, v54, v236 dst_sel:DWORD dst_unused:UNUSED_PAD src0_sel:WORD_1 src1_sel:DWORD
	v_cvt_pk_fp8_f32 v21, v54, v56
	v_and_b32_sdwa v49, v57, v236 dst_sel:DWORD dst_unused:UNUSED_PAD src0_sel:WORD_1 src1_sel:DWORD
	v_and_b32_sdwa v58, v56, v236 dst_sel:DWORD dst_unused:UNUSED_PAD src0_sel:WORD_1 src1_sel:DWORD
	v_and_b32_sdwa v25, v55, v236 dst_sel:DWORD dst_unused:UNUSED_PAD src0_sel:WORD_1 src1_sel:DWORD
	v_add3_u32 v27, v54, v27, s80
	v_add3_u32 v49, v57, v49, s80
	v_add3_u32 v54, v56, v58, s80
	v_cvt_pk_fp8_f32 v21, v55, v57 op_sel:[0,0,1]
	v_add3_u32 v25, v55, v25, s80
	v_and_b32_e32 v49, 0xffff0000, v49
	v_and_b32_e32 v54, 0xffff0000, v54
	v_or_b32_sdwa v55, v49, v25 dst_sel:DWORD dst_unused:UNUSED_PAD src0_sel:DWORD src1_sel:WORD_1
	v_or_b32_sdwa v54, v54, v27 dst_sel:DWORD dst_unused:UNUSED_PAD src0_sel:DWORD src1_sel:WORD_1
	global_store_dwordx2 v[50:51], v[54:55], off offset:1024
	global_store_dword v[52:53], v21, off offset:512
	s_nop 0
	v_mov_b32_e32 v66, v2
	v_mov_b32_e32 v67, v4
	v_mov_b32_e32 v68, v3
	v_mov_b32_e32 v69, v5
	v_pk_mul_f32 v[66:67], v[66:67], v[48:49] op_sel_hi:[1,0]
	v_pk_mul_f32 v[68:69], v[68:69], v[48:49] op_sel_hi:[1,0]
	v_mov_b32_e32 v19, v1
	s_mov_b64 s[8:9], 0
	s_waitcnt vmcnt(2)
	v_mov_b64_e32 v[54:55], v[206:207]
	v_mov_b64_e32 v[56:57], v[208:209]
	v_mov_b32_e32 v70, v54
	v_mov_b32_e32 v71, v56
	s_waitcnt vmcnt(1)
	v_mov_b64_e32 v[58:59], v[210:211]
	v_mov_b64_e32 v[60:61], v[212:213]
	v_mov_b32_e32 v72, v58
	v_mov_b32_e32 v73, v60
	v_mov_b32_e32 v56, v55
	v_mov_b32_e32 v60, v59
	s_waitcnt vmcnt(0)
	v_mov_b64_e32 v[62:63], v[228:229]
	v_mov_b64_e32 v[64:65], v[230:231]
	v_mov_b32_e32 v74, v62
	v_mov_b32_e32 v75, v64
	v_mov_b32_e32 v64, v63
	v_pk_mul_f32 v[54:55], v[66:67], v[70:71]
	v_pk_add_f32 v[58:59], v[72:73], 1.0 op_sel_hi:[1,0]
	v_pk_mul_f32 v[56:57], v[68:69], v[56:57]
	v_pk_add_f32 v[60:61], v[60:61], 1.0 op_sel_hi:[1,0]
	v_pk_fma_f32 v[54:55], v[54:55], v[58:59], v[74:75]
	v_pk_fma_f32 v[56:57], v[56:57], v[60:61], v[64:65]
	v_and_b32_sdwa v21, v55, v236 dst_sel:DWORD dst_unused:UNUSED_PAD src0_sel:WORD_1 src1_sel:DWORD
	v_cvt_pk_fp8_f32 v19, v54, v56
	v_and_b32_sdwa v27, v57, v236 dst_sel:DWORD dst_unused:UNUSED_PAD src0_sel:WORD_1 src1_sel:DWORD
	v_and_b32_sdwa v49, v56, v236 dst_sel:DWORD dst_unused:UNUSED_PAD src0_sel:WORD_1 src1_sel:DWORD
	v_and_b32_sdwa v25, v54, v236 dst_sel:DWORD dst_unused:UNUSED_PAD src0_sel:WORD_1 src1_sel:DWORD
	v_add3_u32 v27, v57, v27, s80
	v_add3_u32 v49, v56, v49, s80
	v_cvt_pk_fp8_f32 v19, v55, v57 op_sel:[0,0,1]
	v_add3_u32 v25, v54, v25, s80
	v_add3_u32 v21, v55, v21, s80
	v_and_b32_e32 v27, 0xffff0000, v27
	v_and_b32_e32 v49, 0xffff0000, v49
	v_or_b32_sdwa v55, v27, v21 dst_sel:DWORD dst_unused:UNUSED_PAD src0_sel:DWORD src1_sel:WORD_1
	v_or_b32_sdwa v54, v49, v25 dst_sel:DWORD dst_unused:UNUSED_PAD src0_sel:DWORD src1_sel:WORD_1
	global_store_dwordx2 v[50:51], v[54:55], off offset:1536
	global_store_dword v[52:53], v19, off offset:768
.LBB0_2168:
	s_andn2_b64 vcc, exec, s[8:9]
	s_cbranch_vccnz .LBB0_2150
	global_load_dwordx4 v[50:53], v[30:31], off
	global_load_dwordx4 v[170:173], v[30:31], off offset:1024
	global_load_dwordx4 v[174:177], v[30:31], off offset:2048
	global_load_dwordx4 v[178:181], v[30:31], off offset:3072
	v_pk_mul_f32 v[6:7], v[6:7], v[48:49] op_sel_hi:[1,0]
	v_pk_mul_f32 v[8:9], v[8:9], v[48:49] op_sel_hi:[1,0]
	v_lshl_add_u64 v[54:55], s[10:11], 2, v[38:39]
	v_pk_mul_f32 v[10:11], v[10:11], v[48:49] op_sel_hi:[1,0]
	v_pk_mul_f32 v[12:13], v[12:13], v[48:49] op_sel_hi:[1,0]
	v_pk_mul_f32 v[2:3], v[2:3], v[48:49] op_sel_hi:[1,0]
	v_pk_mul_f32 v[4:5], v[4:5], v[48:49] op_sel_hi:[1,0]
	s_waitcnt vmcnt(0)
	v_pk_mul_f32 v[6:7], v[6:7], v[50:51]
	v_pk_mul_f32 v[8:9], v[8:9], v[52:53]
	global_store_dwordx4 v[54:55], v[6:9], off
	s_waitcnt vmcnt(0)
	v_mov_b64_e32 v[6:7], v[170:171]
	v_mov_b64_e32 v[8:9], v[172:173]
	v_pk_mul_f32 v[6:7], v[10:11], v[6:7]
	v_pk_mul_f32 v[8:9], v[12:13], v[8:9]
	global_store_dwordx4 v[54:55], v[6:9], off offset:1024
	v_pk_mul_f32 v[10:11], v[14:15], v[48:49] op_sel_hi:[1,0]
	v_pk_mul_f32 v[12:13], v[16:17], v[48:49] op_sel_hi:[1,0]
	s_waitcnt vmcnt(0)
	v_mov_b64_e32 v[6:7], v[174:175]
	v_mov_b64_e32 v[8:9], v[176:177]
	v_pk_mul_f32 v[6:7], v[10:11], v[6:7]
	v_pk_mul_f32 v[8:9], v[12:13], v[8:9]
	global_store_dwordx4 v[54:55], v[6:9], off offset:2048
	s_waitcnt vmcnt(0)
	v_mov_b64_e32 v[6:7], v[178:179]
	v_mov_b64_e32 v[8:9], v[180:181]
	v_pk_mul_f32 v[2:3], v[2:3], v[6:7]
	v_pk_mul_f32 v[4:5], v[4:5], v[8:9]
	global_store_dwordx4 v[54:55], v[2:5], off offset:3072
	s_branch .LBB0_2150
